# write-through (sc0 sc1) stores for Z, Y2 and Z1 in the GEMM epilogues, so the seam release has less to write back
# speedup vs baseline: 1.0181x; 1.0024x over previous
;     __device__ __forceinline__ void operator()() { if (cnt == turn) run_all(tid_); ++cnt; }
;     __device__ __forceinline__ void operator()(const Acc& acc, const Unit& u, int wr, int wc, int fr, int fq) const {
;         const int row0 = u.pm * BM + wr * 64 + fr, col0 = u.pn * BM + wc * 32 + 8 * fq;
;         const float sc = (u.pn < 4) ? QSCALE : 1.f;
;         const bool dorope = (u.pn == 2 || u.pn == 3 || u.pn == 6 || u.pn == 7) && (u.pm * BM < NTOK);
; #pragma unroll
;         for (int ai = 0; ai < 2; ++ai)
; #pragma unroll
;             for (int m = 0; m < 4; ++m) { const int row = row0 + ai * HALF + m * 16; f16* rowp = O + (size_t)row * ZP0 + col0;
;                 const int t = row & (SEQ - 1), prow = t >> 6, pcol = t & 63;
; #pragma unroll
;                 for (int bj = 0; bj < 2; ++bj) { f32x4 v0 = acc[ai][bj][m][0] * sc, v1 = acc[ai][bj][m][1] * sc;
;                     if (dorope) { const int c = col0 + bj * HALF, half = (c >> 5) & 1, i0 = (c & 31) >> 1; const int pos = half ? pcol : prow;
;                         const f32x4* tp = (const f32x4*)(rope + (pos * 16 + i0) * 2); const f32x4 t0 = tp[0], t1 = tp[1];
;                         f32x4 r0, r1;
;                         r0[0] = v0[0] * t0[0] - v0[1] * t0[1]; r0[1] = v0[0] * t0[1] + v0[1] * t0[0];
;                         r0[2] = v0[2] * t0[2] - v0[3] * t0[3]; r0[3] = v0[2] * t0[3] + v0[3] * t0[2];
;                         r1[0] = v1[0] * t1[0] - v1[1] * t1[1]; r1[1] = v1[0] * t1[1] + v1[1] * t1[0];
;                         r1[2] = v1[2] * t1[2] - v1[3] * t1[3]; r1[3] = v1[2] * t1[3] + v1[3] * t1[2];
;                         v0 = r0; v1 = r1; }
;                     u32x4 w; w.x = pkh(v0[0], v0[1]); w.y = pkh(v0[2], v0[3]); w.z = pkh(v1[0], v1[1]); w.w = pkh(v1[2], v1[3]);
;                     *(u32x4*)(rowp + bj * HALF) = w; } }
.LBB0_391:
	v_or_b32_e32 v162, s21, v1
	v_lshl_or_b32 v122, s26, 8, v157
	v_mov_b64_e32 v[126:127], s[76:77]
	v_mov_b32_e32 v147, v146
	v_ashrrev_i32_e32 v123, 31, v122
	v_mad_i64_i32 v[126:127], s[2:3], v162, s47, v[126:127]
	v_cvt_pk_f16_f32 v167, v124, v125
	v_mov_b32_e32 v124, v146
	v_mov_b32_e32 v125, v146
	v_lshl_add_u64 v[126:127], v[122:123], 1, v[126:127]
	v_cvt_pk_f16_f32 v164, v128, v129
	v_cvt_pk_f16_f32 v165, v150, v151
	v_cvt_pk_f16_f32 v166, v148, v149
	v_pk_mul_f32 v[120:121], v[124:125], v[120:121]
	v_pk_mul_f32 v[118:119], v[146:147], v[118:119]
	v_pk_mul_f32 v[116:117], v[124:125], v[116:117]
	s_and_b64 vcc, exec, s[8:9]
	v_pk_mul_f32 v[114:115], v[146:147], v[114:115]
	global_store_dwordx4 v[126:127], v[164:167], off sc0 sc1
	s_cbranch_vccnz .LBB0_393
	v_lshlrev_b32_e32 v128, 2, v163
	global_load_dwordx4 v[148:151], v128, s[12:13]
	global_load_dwordx4 v[164:167], v128, s[12:13] offset:16
	s_waitcnt vmcnt(0)
	v_pk_mul_f32 v[168:169], v[118:119], v[148:149] op_sel:[1,1] op_sel_hi:[1,0]
	v_mul_f32_e32 v170, v121, v151
	v_mul_f32_e32 v172, v121, v150
	v_pk_mul_f32 v[176:177], v[114:115], v[164:165] op_sel:[1,1] op_sel_hi:[1,0]
	v_mul_f32_e32 v178, v117, v167
	v_mul_f32_e32 v180, v117, v166
	v_pk_mul_f32 v[128:129], v[118:119], v[148:149]
	v_pk_mul_f32 v[174:175], v[114:115], v[164:165]
	v_pk_fma_f32 v[118:119], v[118:119], v[148:149], v[168:169] op_sel_hi:[0,1,1]
	v_pk_fma_f32 v[148:149], v[120:121], v[150:151], v[170:171] op_sel_hi:[1,1,0] neg_lo:[0,0,1] neg_hi:[0,0,1]
	v_pk_fma_f32 v[150:151], v[120:121], v[150:151], v[172:173] op_sel:[0,1,0] op_sel_hi:[1,0,0]
	v_pk_fma_f32 v[114:115], v[114:115], v[164:165], v[176:177] op_sel_hi:[0,1,1]
	v_pk_fma_f32 v[120:121], v[116:117], v[166:167], v[178:179] op_sel_hi:[1,1,0] neg_lo:[0,0,1] neg_hi:[0,0,1]
	v_pk_fma_f32 v[164:165], v[116:117], v[166:167], v[180:181] op_sel:[0,1,0] op_sel_hi:[1,0,0]
	v_sub_f32_e32 v114, v174, v176
	v_sub_f32_e32 v118, v128, v168
	v_mov_b32_e32 v116, v120
	v_mov_b32_e32 v117, v164
	v_mov_b32_e32 v120, v148
	v_mov_b32_e32 v121, v150
.LBB0_393:
	v_cvt_pk_f16_f32 v118, v118, v119
	v_cvt_pk_f16_f32 v119, v120, v121
	v_cvt_pk_f16_f32 v120, v114, v115
	v_mov_b32_e32 v114, s19
	v_cndmask_b32_e64 v114, v154, v114, s[4:5]
	v_cvt_pk_f16_f32 v121, v116, v117
	v_lshl_or_b32 v116, v114, 5, v152
	v_pk_mul_f32 v[114:115], v[124:125], v[112:113]
	v_pk_mul_f32 v[110:111], v[146:147], v[110:111]
	v_pk_mul_f32 v[112:113], v[124:125], v[108:109]
	s_and_b64 vcc, exec, s[8:9]
	v_pk_mul_f32 v[106:107], v[146:147], v[106:107]
	global_store_dwordx4 v[126:127], v[118:121], off offset:256 sc0 sc1
	s_cbranch_vccnz .LBB0_395
	v_lshlrev_b32_e32 v108, 2, v116
	global_load_dwordx4 v[118:121], v108, s[12:13]
	global_load_dwordx4 v[124:127], v108, s[12:13] offset:16
	s_waitcnt vmcnt(0)
	v_pk_mul_f32 v[128:129], v[110:111], v[118:119] op_sel:[1,1] op_sel_hi:[1,0]
	v_mul_f32_e32 v148, v115, v121
	v_mul_f32_e32 v150, v115, v120
	v_pk_mul_f32 v[166:167], v[106:107], v[124:125] op_sel:[1,1] op_sel_hi:[1,0]
	v_mul_f32_e32 v168, v113, v127
	v_mul_f32_e32 v170, v113, v126
	v_pk_mul_f32 v[108:109], v[110:111], v[118:119]
	v_pk_mul_f32 v[164:165], v[106:107], v[124:125]
	v_pk_fma_f32 v[110:111], v[110:111], v[118:119], v[128:129] op_sel_hi:[0,1,1]
	v_pk_fma_f32 v[118:119], v[114:115], v[120:121], v[148:149] op_sel_hi:[1,1,0] neg_lo:[0,0,1] neg_hi:[0,0,1]
	v_pk_fma_f32 v[120:121], v[114:115], v[120:121], v[150:151] op_sel:[0,1,0] op_sel_hi:[1,0,0]
	v_pk_fma_f32 v[106:107], v[106:107], v[124:125], v[166:167] op_sel_hi:[0,1,1]
	v_pk_fma_f32 v[114:115], v[112:113], v[126:127], v[168:169] op_sel_hi:[1,1,0] neg_lo:[0,0,1] neg_hi:[0,0,1]
	v_pk_fma_f32 v[124:125], v[112:113], v[126:127], v[170:171] op_sel:[0,1,0] op_sel_hi:[1,0,0]
	v_sub_f32_e32 v106, v164, v166
	v_sub_f32_e32 v110, v108, v128
	v_mov_b32_e32 v112, v114
	v_mov_b32_e32 v113, v124
	v_mov_b32_e32 v114, v118
	v_mov_b32_e32 v115, v120
.LBB0_395:
	v_or_b32_e32 v117, 16, v162
	v_mov_b64_e32 v[108:109], s[76:77]
	v_mad_i64_i32 v[108:109], s[2:3], v117, s47, v[108:109]
	v_cvt_pk_f16_f32 v120, v106, v107
	v_mov_b32_e32 v106, v146
	v_mov_b32_e32 v107, v146
	v_lshl_add_u64 v[108:109], v[122:123], 1, v[108:109]
	v_cvt_pk_f16_f32 v118, v110, v111
	v_cvt_pk_f16_f32 v119, v114, v115
	v_cvt_pk_f16_f32 v121, v112, v113
	v_pk_mul_f32 v[104:105], v[106:107], v[104:105]
	v_pk_mul_f32 v[102:103], v[146:147], v[102:103]
	v_pk_mul_f32 v[100:101], v[106:107], v[100:101]
	s_and_b64 vcc, exec, s[8:9]
	v_pk_mul_f32 v[98:99], v[146:147], v[98:99]
	global_store_dwordx4 v[108:109], v[118:121], off sc0 sc1
	s_cbranch_vccnz .LBB0_397
	v_lshlrev_b32_e32 v114, 2, v116
	global_load_dwordx4 v[110:113], v114, s[12:13]
	s_nop 0
	global_load_dwordx4 v[114:117], v114, s[12:13] offset:16
	s_waitcnt vmcnt(0)
	v_pk_mul_f32 v[120:121], v[102:103], v[110:111] op_sel:[1,1] op_sel_hi:[1,0]
	v_mul_f32_e32 v124, v105, v113
	v_mul_f32_e32 v126, v105, v112
	v_pk_mul_f32 v[148:149], v[98:99], v[114:115] op_sel:[1,1] op_sel_hi:[1,0]
	v_mul_f32_e32 v150, v101, v117
	v_mul_f32_e32 v164, v101, v116
	v_pk_mul_f32 v[118:119], v[102:103], v[110:111]
	v_pk_mul_f32 v[128:129], v[98:99], v[114:115]
	v_pk_fma_f32 v[102:103], v[102:103], v[110:111], v[120:121] op_sel_hi:[0,1,1]
	v_pk_fma_f32 v[110:111], v[104:105], v[112:113], v[124:125] op_sel_hi:[1,1,0] neg_lo:[0,0,1] neg_hi:[0,0,1]
	v_pk_fma_f32 v[112:113], v[104:105], v[112:113], v[126:127] op_sel:[0,1,0] op_sel_hi:[1,0,0]
	v_pk_fma_f32 v[98:99], v[98:99], v[114:115], v[148:149] op_sel_hi:[0,1,1]
	v_pk_fma_f32 v[104:105], v[100:101], v[116:117], v[150:151] op_sel_hi:[1,1,0] neg_lo:[0,0,1] neg_hi:[0,0,1]
	v_pk_fma_f32 v[114:115], v[100:101], v[116:117], v[164:165] op_sel:[0,1,0] op_sel_hi:[1,0,0]
	v_sub_f32_e32 v98, v128, v148
	v_sub_f32_e32 v102, v118, v120
	v_mov_b32_e32 v100, v104
	v_mov_b32_e32 v101, v114
	v_mov_b32_e32 v104, v110
	v_mov_b32_e32 v105, v112
;     __device__ __forceinline__ void operator()(const Acc& acc, const Unit& u, int wr, int wc, int fr, int fq) const {
;     ...
;             for (int m = 0; m < 4; ++m) { const int row = row0 + ai * HALF + m * 16; f16* rowp = O + (size_t)row * ZP0 + col0;
;                 const int t = row & (SEQ - 1), prow = t >> 6, pcol = t & 63;
; #pragma unroll
;                 for (int bj = 0; bj < 2; ++bj) { f32x4 v0 = acc[ai][bj][m][0] * sc, v1 = acc[ai][bj][m][1] * sc;
;                     if (dorope) { const int c = col0 + bj * HALF, half = (c >> 5) & 1, i0 = (c & 31) >> 1; const int pos = half ? pcol : prow;
;                         const f32x4* tp = (const f32x4*)(rope + (pos * 16 + i0) * 2); const f32x4 t0 = tp[0], t1 = tp[1];
;                         f32x4 r0, r1;
;                         r0[0] = v0[0] * t0[0] - v0[1] * t0[1]; r0[1] = v0[0] * t0[1] + v0[1] * t0[0];
;                         r0[2] = v0[2] * t0[2] - v0[3] * t0[3]; r0[3] = v0[2] * t0[3] + v0[3] * t0[2];
;                         r1[0] = v1[0] * t1[0] - v1[1] * t1[1]; r1[1] = v1[0] * t1[1] + v1[1] * t1[0];
;                         r1[2] = v1[2] * t1[2] - v1[3] * t1[3]; r1[3] = v1[2] * t1[3] + v1[3] * t1[2];
;                         v0 = r0; v1 = r1; }
;                     u32x4 w; w.x = pkh(v0[0], v0[1]); w.y = pkh(v0[2], v0[3]); w.z = pkh(v1[0], v1[1]); w.w = pkh(v1[2], v1[3]);
;                     *(u32x4*)(rowp + bj * HALF) = w; } }
.LBB0_397:
	v_cvt_pk_f16_f32 v102, v102, v103
	v_cvt_pk_f16_f32 v103, v104, v105
	v_cvt_pk_f16_f32 v104, v98, v99
	v_mov_b32_e32 v98, s19
	v_cndmask_b32_e64 v98, v155, v98, s[4:5]
	v_cvt_pk_f16_f32 v105, v100, v101
	v_lshl_or_b32 v100, v98, 5, v152
	v_pk_mul_f32 v[98:99], v[106:107], v[96:97]
	v_pk_mul_f32 v[94:95], v[146:147], v[94:95]
	v_pk_mul_f32 v[96:97], v[106:107], v[92:93]
	s_and_b64 vcc, exec, s[8:9]
	v_pk_mul_f32 v[90:91], v[146:147], v[90:91]
	global_store_dwordx4 v[108:109], v[102:105], off offset:256 sc0 sc1
	s_cbranch_vccnz .LBB0_399
	v_lshlrev_b32_e32 v92, 2, v100
	global_load_dwordx4 v[102:105], v92, s[12:13]
	global_load_dwordx4 v[106:109], v92, s[12:13] offset:16
	s_waitcnt vmcnt(0)
	v_pk_mul_f32 v[110:111], v[94:95], v[102:103] op_sel:[1,1] op_sel_hi:[1,0]
	v_mul_f32_e32 v112, v99, v105
	v_mul_f32_e32 v114, v99, v104
	v_pk_mul_f32 v[118:119], v[90:91], v[106:107] op_sel:[1,1] op_sel_hi:[1,0]
	v_mul_f32_e32 v120, v97, v109
	v_mul_f32_e32 v124, v97, v108
	v_pk_mul_f32 v[92:93], v[94:95], v[102:103]
	v_pk_mul_f32 v[116:117], v[90:91], v[106:107]
	v_pk_fma_f32 v[94:95], v[94:95], v[102:103], v[110:111] op_sel_hi:[0,1,1]
	v_pk_fma_f32 v[102:103], v[98:99], v[104:105], v[112:113] op_sel_hi:[1,1,0] neg_lo:[0,0,1] neg_hi:[0,0,1]
	v_pk_fma_f32 v[104:105], v[98:99], v[104:105], v[114:115] op_sel:[0,1,0] op_sel_hi:[1,0,0]
	v_pk_fma_f32 v[90:91], v[90:91], v[106:107], v[118:119] op_sel_hi:[0,1,1]
	v_pk_fma_f32 v[98:99], v[96:97], v[108:109], v[120:121] op_sel_hi:[1,1,0] neg_lo:[0,0,1] neg_hi:[0,0,1]
	v_pk_fma_f32 v[106:107], v[96:97], v[108:109], v[124:125] op_sel:[0,1,0] op_sel_hi:[1,0,0]
	v_sub_f32_e32 v90, v116, v118
	v_sub_f32_e32 v94, v92, v110
	v_mov_b32_e32 v96, v98
	v_mov_b32_e32 v97, v106
	v_mov_b32_e32 v98, v102
	v_mov_b32_e32 v99, v104
.LBB0_399:
	v_or_b32_e32 v101, 32, v162
	v_mov_b64_e32 v[92:93], s[76:77]
	v_mad_i64_i32 v[92:93], s[2:3], v101, s47, v[92:93]
	v_cvt_pk_f16_f32 v104, v90, v91
	v_mov_b32_e32 v90, v146
	v_mov_b32_e32 v91, v146
	v_lshl_add_u64 v[92:93], v[122:123], 1, v[92:93]
	v_cvt_pk_f16_f32 v102, v94, v95
	v_cvt_pk_f16_f32 v103, v98, v99
	v_cvt_pk_f16_f32 v105, v96, v97
	v_pk_mul_f32 v[88:89], v[90:91], v[88:89]
	v_pk_mul_f32 v[86:87], v[146:147], v[86:87]
	v_pk_mul_f32 v[84:85], v[90:91], v[84:85]
	s_and_b64 vcc, exec, s[8:9]
	v_pk_mul_f32 v[82:83], v[146:147], v[82:83]
	global_store_dwordx4 v[92:93], v[102:105], off sc0 sc1
	s_cbranch_vccnz .LBB0_401
	v_lshlrev_b32_e32 v98, 2, v100
	global_load_dwordx4 v[94:97], v98, s[12:13]
	s_nop 0
	global_load_dwordx4 v[98:101], v98, s[12:13] offset:16
	s_waitcnt vmcnt(0)
	v_pk_mul_f32 v[104:105], v[86:87], v[94:95] op_sel:[1,1] op_sel_hi:[1,0]
	v_mul_f32_e32 v106, v89, v97
	v_mul_f32_e32 v108, v89, v96
	v_pk_mul_f32 v[112:113], v[82:83], v[98:99] op_sel:[1,1] op_sel_hi:[1,0]
	v_mul_f32_e32 v114, v85, v101
	v_mul_f32_e32 v116, v85, v100
	v_pk_mul_f32 v[102:103], v[86:87], v[94:95]
	v_pk_mul_f32 v[110:111], v[82:83], v[98:99]
	v_pk_fma_f32 v[86:87], v[86:87], v[94:95], v[104:105] op_sel_hi:[0,1,1]
	v_pk_fma_f32 v[94:95], v[88:89], v[96:97], v[106:107] op_sel_hi:[1,1,0] neg_lo:[0,0,1] neg_hi:[0,0,1]
	v_pk_fma_f32 v[96:97], v[88:89], v[96:97], v[108:109] op_sel:[0,1,0] op_sel_hi:[1,0,0]
	v_pk_fma_f32 v[82:83], v[82:83], v[98:99], v[112:113] op_sel_hi:[0,1,1]
	v_pk_fma_f32 v[88:89], v[84:85], v[100:101], v[114:115] op_sel_hi:[1,1,0] neg_lo:[0,0,1] neg_hi:[0,0,1]
	v_pk_fma_f32 v[98:99], v[84:85], v[100:101], v[116:117] op_sel:[0,1,0] op_sel_hi:[1,0,0]
	v_sub_f32_e32 v82, v110, v112
	v_sub_f32_e32 v86, v102, v104
	v_mov_b32_e32 v84, v88
	v_mov_b32_e32 v85, v98
	v_mov_b32_e32 v88, v94
	v_mov_b32_e32 v89, v96
.LBB0_401:
	v_cvt_pk_f16_f32 v86, v86, v87
	v_cvt_pk_f16_f32 v87, v88, v89
	v_cvt_pk_f16_f32 v88, v82, v83
	v_mov_b32_e32 v82, s19
	v_cndmask_b32_e64 v82, v156, v82, s[4:5]
	v_cvt_pk_f16_f32 v89, v84, v85
	v_lshl_or_b32 v84, v82, 5, v152
	v_pk_mul_f32 v[82:83], v[90:91], v[80:81]
	v_pk_mul_f32 v[78:79], v[146:147], v[78:79]
	v_pk_mul_f32 v[80:81], v[90:91], v[76:77]
	s_and_b64 vcc, exec, s[8:9]
	v_pk_mul_f32 v[74:75], v[146:147], v[74:75]
	global_store_dwordx4 v[92:93], v[86:89], off offset:256 sc0 sc1
	s_cbranch_vccnz .LBB0_403
	v_lshlrev_b32_e32 v76, 2, v84
	global_load_dwordx4 v[86:89], v76, s[12:13]
	global_load_dwordx4 v[90:93], v76, s[12:13] offset:16
	s_waitcnt vmcnt(0)
	v_pk_mul_f32 v[94:95], v[78:79], v[86:87] op_sel:[1,1] op_sel_hi:[1,0]
	v_mul_f32_e32 v96, v83, v89
	v_mul_f32_e32 v98, v83, v88
	v_pk_mul_f32 v[102:103], v[74:75], v[90:91] op_sel:[1,1] op_sel_hi:[1,0]
	v_mul_f32_e32 v104, v81, v93
	v_mul_f32_e32 v106, v81, v92
	v_pk_mul_f32 v[76:77], v[78:79], v[86:87]
	v_pk_mul_f32 v[100:101], v[74:75], v[90:91]
	v_pk_fma_f32 v[78:79], v[78:79], v[86:87], v[94:95] op_sel_hi:[0,1,1]
	v_pk_fma_f32 v[86:87], v[82:83], v[88:89], v[96:97] op_sel_hi:[1,1,0] neg_lo:[0,0,1] neg_hi:[0,0,1]
	v_pk_fma_f32 v[88:89], v[82:83], v[88:89], v[98:99] op_sel:[0,1,0] op_sel_hi:[1,0,0]
	v_pk_fma_f32 v[74:75], v[74:75], v[90:91], v[102:103] op_sel_hi:[0,1,1]
	v_pk_fma_f32 v[82:83], v[80:81], v[92:93], v[104:105] op_sel_hi:[1,1,0] neg_lo:[0,0,1] neg_hi:[0,0,1]
	v_pk_fma_f32 v[90:91], v[80:81], v[92:93], v[106:107] op_sel:[0,1,0] op_sel_hi:[1,0,0]
	v_sub_f32_e32 v74, v100, v102
	v_sub_f32_e32 v78, v76, v94
	v_mov_b32_e32 v80, v82
	v_mov_b32_e32 v81, v90
	v_mov_b32_e32 v82, v86
	v_mov_b32_e32 v83, v88
;     __device__ __forceinline__ void operator()(const Acc& acc, const Unit& u, int wr, int wc, int fr, int fq) const {
;     ...
;             for (int m = 0; m < 4; ++m) { const int row = row0 + ai * HALF + m * 16; f16* rowp = O + (size_t)row * ZP0 + col0;
;                 const int t = row & (SEQ - 1), prow = t >> 6, pcol = t & 63;
; #pragma unroll
;                 for (int bj = 0; bj < 2; ++bj) { f32x4 v0 = acc[ai][bj][m][0] * sc, v1 = acc[ai][bj][m][1] * sc;
;                     if (dorope) { const int c = col0 + bj * HALF, half = (c >> 5) & 1, i0 = (c & 31) >> 1; const int pos = half ? pcol : prow;
;                         const f32x4* tp = (const f32x4*)(rope + (pos * 16 + i0) * 2); const f32x4 t0 = tp[0], t1 = tp[1];
;                         f32x4 r0, r1;
;                         r0[0] = v0[0] * t0[0] - v0[1] * t0[1]; r0[1] = v0[0] * t0[1] + v0[1] * t0[0];
;                         r0[2] = v0[2] * t0[2] - v0[3] * t0[3]; r0[3] = v0[2] * t0[3] + v0[3] * t0[2];
;                         r1[0] = v1[0] * t1[0] - v1[1] * t1[1]; r1[1] = v1[0] * t1[1] + v1[1] * t1[0];
;                         r1[2] = v1[2] * t1[2] - v1[3] * t1[3]; r1[3] = v1[2] * t1[3] + v1[3] * t1[2];
;                         v0 = r0; v1 = r1; }
;                     u32x4 w; w.x = pkh(v0[0], v0[1]); w.y = pkh(v0[2], v0[3]); w.z = pkh(v1[0], v1[1]); w.w = pkh(v1[2], v1[3]);
;                     *(u32x4*)(rowp + bj * HALF) = w; } }
.LBB0_403:
	v_or_b32_e32 v85, 48, v162
	v_mov_b64_e32 v[76:77], s[76:77]
	v_mad_i64_i32 v[76:77], s[2:3], v85, s47, v[76:77]
	v_cvt_pk_f16_f32 v88, v74, v75
	v_mov_b32_e32 v74, v146
	v_mov_b32_e32 v75, v146
	v_lshl_add_u64 v[76:77], v[122:123], 1, v[76:77]
	v_cvt_pk_f16_f32 v86, v78, v79
	v_cvt_pk_f16_f32 v87, v82, v83
	v_cvt_pk_f16_f32 v89, v80, v81
	v_pk_mul_f32 v[72:73], v[74:75], v[72:73]
	v_pk_mul_f32 v[70:71], v[146:147], v[70:71]
	v_pk_mul_f32 v[68:69], v[74:75], v[68:69]
	s_and_b64 vcc, exec, s[8:9]
	v_pk_mul_f32 v[66:67], v[146:147], v[66:67]
	global_store_dwordx4 v[76:77], v[86:89], off sc0 sc1
	s_cbranch_vccnz .LBB0_405
	v_lshlrev_b32_e32 v82, 2, v84
	global_load_dwordx4 v[78:81], v82, s[12:13]
	s_nop 0
	global_load_dwordx4 v[82:85], v82, s[12:13] offset:16
	s_waitcnt vmcnt(0)
	v_pk_mul_f32 v[88:89], v[70:71], v[78:79] op_sel:[1,1] op_sel_hi:[1,0]
	v_mul_f32_e32 v90, v73, v81
	v_mul_f32_e32 v92, v73, v80
	v_pk_mul_f32 v[96:97], v[66:67], v[82:83] op_sel:[1,1] op_sel_hi:[1,0]
	v_mul_f32_e32 v98, v69, v85
	v_mul_f32_e32 v100, v69, v84
	v_pk_mul_f32 v[86:87], v[70:71], v[78:79]
	v_pk_mul_f32 v[94:95], v[66:67], v[82:83]
	v_pk_fma_f32 v[70:71], v[70:71], v[78:79], v[88:89] op_sel_hi:[0,1,1]
	v_pk_fma_f32 v[78:79], v[72:73], v[80:81], v[90:91] op_sel_hi:[1,1,0] neg_lo:[0,0,1] neg_hi:[0,0,1]
	v_pk_fma_f32 v[80:81], v[72:73], v[80:81], v[92:93] op_sel:[0,1,0] op_sel_hi:[1,0,0]
	v_pk_fma_f32 v[66:67], v[66:67], v[82:83], v[96:97] op_sel_hi:[0,1,1]
	v_pk_fma_f32 v[72:73], v[68:69], v[84:85], v[98:99] op_sel_hi:[1,1,0] neg_lo:[0,0,1] neg_hi:[0,0,1]
	v_pk_fma_f32 v[82:83], v[68:69], v[84:85], v[100:101] op_sel:[0,1,0] op_sel_hi:[1,0,0]
	v_sub_f32_e32 v66, v94, v96
	v_sub_f32_e32 v70, v86, v88
	v_mov_b32_e32 v68, v72
	v_mov_b32_e32 v69, v82
	v_mov_b32_e32 v72, v78
	v_mov_b32_e32 v73, v80
.LBB0_405:
	v_cvt_pk_f16_f32 v70, v70, v71
	v_cvt_pk_f16_f32 v71, v72, v73
	v_cvt_pk_f16_f32 v72, v66, v67
	v_cvt_pk_f16_f32 v73, v68, v69
	global_store_dwordx4 v[76:77], v[70:73], off offset:256 sc0 sc1
	v_pk_mul_f32 v[62:63], v[146:147], v[62:63]
	s_and_b64 vcc, exec, s[8:9]
	v_add_u32_e32 v70, 0x80, v162
	v_bfe_u32 v68, v70, 6, 5
	v_cndmask_b32_e64 v66, v1, v68, s[4:5]
	v_lshl_or_b32 v69, v66, 5, v152
	v_pk_mul_f32 v[66:67], v[74:75], v[64:65]
	v_pk_mul_f32 v[64:65], v[74:75], v[60:61]
	v_pk_mul_f32 v[60:61], v[146:147], v[58:59]
	s_cbranch_vccnz .LBB0_407
	v_lshlrev_b32_e32 v58, 2, v69
	global_load_dwordx4 v[72:75], v58, s[12:13]
	global_load_dwordx4 v[76:79], v58, s[12:13] offset:16
	s_waitcnt vmcnt(0)
	v_pk_mul_f32 v[80:81], v[62:63], v[72:73] op_sel:[1,1] op_sel_hi:[1,0]
	v_mul_f32_e32 v82, v67, v75
	v_mul_f32_e32 v84, v67, v74
	v_pk_mul_f32 v[88:89], v[60:61], v[76:77] op_sel:[1,1] op_sel_hi:[1,0]
	v_mul_f32_e32 v90, v65, v79
	v_mul_f32_e32 v92, v65, v78
	v_pk_mul_f32 v[58:59], v[62:63], v[72:73]
	v_pk_mul_f32 v[86:87], v[60:61], v[76:77]
	v_pk_fma_f32 v[62:63], v[62:63], v[72:73], v[80:81] op_sel_hi:[0,1,1]
	v_pk_fma_f32 v[72:73], v[66:67], v[74:75], v[82:83] op_sel_hi:[1,1,0] neg_lo:[0,0,1] neg_hi:[0,0,1]
	v_pk_fma_f32 v[74:75], v[66:67], v[74:75], v[84:85] op_sel:[0,1,0] op_sel_hi:[1,0,0]
	v_pk_fma_f32 v[60:61], v[60:61], v[76:77], v[88:89] op_sel_hi:[0,1,1]
	v_pk_fma_f32 v[66:67], v[64:65], v[78:79], v[90:91] op_sel_hi:[1,1,0] neg_lo:[0,0,1] neg_hi:[0,0,1]
	v_pk_fma_f32 v[76:77], v[64:65], v[78:79], v[92:93] op_sel:[0,1,0] op_sel_hi:[1,0,0]
	v_sub_f32_e32 v60, v86, v88
	v_sub_f32_e32 v62, v58, v80
	v_mov_b32_e32 v64, v66
	v_mov_b32_e32 v65, v76
	v_mov_b32_e32 v66, v72
	v_mov_b32_e32 v67, v74
.LBB0_407:
	v_mov_b64_e32 v[58:59], s[76:77]
	v_mad_i64_i32 v[58:59], s[2:3], v70, s47, v[58:59]
	v_cvt_pk_f16_f32 v72, v60, v61
	v_mov_b32_e32 v60, v146
	v_mov_b32_e32 v61, v146
	v_lshl_add_u64 v[58:59], v[122:123], 1, v[58:59]
	v_cvt_pk_f16_f32 v70, v62, v63
	v_cvt_pk_f16_f32 v71, v66, v67
	v_cvt_pk_f16_f32 v73, v64, v65
	v_pk_mul_f32 v[56:57], v[60:61], v[56:57]
	v_pk_mul_f32 v[54:55], v[146:147], v[54:55]
	v_pk_mul_f32 v[52:53], v[60:61], v[52:53]
	s_and_b64 vcc, exec, s[8:9]
	v_pk_mul_f32 v[50:51], v[146:147], v[50:51]
	global_store_dwordx4 v[58:59], v[70:73], off sc0 sc1
	s_cbranch_vccnz .LBB0_409
	v_lshlrev_b32_e32 v66, 2, v69
	global_load_dwordx4 v[62:65], v66, s[12:13]
	global_load_dwordx4 v[70:73], v66, s[12:13] offset:16
	s_waitcnt vmcnt(0)
	v_pk_mul_f32 v[74:75], v[54:55], v[62:63] op_sel:[1,1] op_sel_hi:[1,0]
	v_mul_f32_e32 v76, v57, v65
	v_mul_f32_e32 v78, v57, v64
	v_pk_mul_f32 v[82:83], v[50:51], v[70:71] op_sel:[1,1] op_sel_hi:[1,0]
	v_mul_f32_e32 v84, v53, v73
	v_mul_f32_e32 v86, v53, v72
	v_pk_mul_f32 v[66:67], v[54:55], v[62:63]
	v_pk_mul_f32 v[80:81], v[50:51], v[70:71]
	v_pk_fma_f32 v[54:55], v[54:55], v[62:63], v[74:75] op_sel_hi:[0,1,1]
	v_pk_fma_f32 v[62:63], v[56:57], v[64:65], v[76:77] op_sel_hi:[1,1,0] neg_lo:[0,0,1] neg_hi:[0,0,1]
	v_pk_fma_f32 v[64:65], v[56:57], v[64:65], v[78:79] op_sel:[0,1,0] op_sel_hi:[1,0,0]
	v_pk_fma_f32 v[50:51], v[50:51], v[70:71], v[82:83] op_sel_hi:[0,1,1]
	v_pk_fma_f32 v[56:57], v[52:53], v[72:73], v[84:85] op_sel_hi:[1,1,0] neg_lo:[0,0,1] neg_hi:[0,0,1]
	v_pk_fma_f32 v[70:71], v[52:53], v[72:73], v[86:87] op_sel:[0,1,0] op_sel_hi:[1,0,0]
	v_sub_f32_e32 v50, v80, v82
	v_sub_f32_e32 v54, v66, v74
	v_mov_b32_e32 v52, v56
	v_mov_b32_e32 v53, v70
	v_mov_b32_e32 v56, v62
	v_mov_b32_e32 v57, v64
;     __device__ __forceinline__ void operator()(const Acc& acc, const Unit& u, int wr, int wc, int fr, int fq) const {
;     ...
;             for (int m = 0; m < 4; ++m) { const int row = row0 + ai * HALF + m * 16; f16* rowp = O + (size_t)row * ZP0 + col0;
;                 const int t = row & (SEQ - 1), prow = t >> 6, pcol = t & 63;
; #pragma unroll
;                 for (int bj = 0; bj < 2; ++bj) { f32x4 v0 = acc[ai][bj][m][0] * sc, v1 = acc[ai][bj][m][1] * sc;
;                     if (dorope) { const int c = col0 + bj * HALF, half = (c >> 5) & 1, i0 = (c & 31) >> 1; const int pos = half ? pcol : prow;
;                         const f32x4* tp = (const f32x4*)(rope + (pos * 16 + i0) * 2); const f32x4 t0 = tp[0], t1 = tp[1];
;                         f32x4 r0, r1;
;                         r0[0] = v0[0] * t0[0] - v0[1] * t0[1]; r0[1] = v0[0] * t0[1] + v0[1] * t0[0];
;                         r0[2] = v0[2] * t0[2] - v0[3] * t0[3]; r0[3] = v0[2] * t0[3] + v0[3] * t0[2];
;                         r1[0] = v1[0] * t1[0] - v1[1] * t1[1]; r1[1] = v1[0] * t1[1] + v1[1] * t1[0];
;                         r1[2] = v1[2] * t1[2] - v1[3] * t1[3]; r1[3] = v1[2] * t1[3] + v1[3] * t1[2];
;                         v0 = r0; v1 = r1; }
;                     u32x4 w; w.x = pkh(v0[0], v0[1]); w.y = pkh(v0[2], v0[3]); w.z = pkh(v1[0], v1[1]); w.w = pkh(v1[2], v1[3]);
;                     *(u32x4*)(rowp + bj * HALF) = w; } }
.LBB0_409:
	v_cvt_pk_f16_f32 v54, v54, v55
	v_cvt_pk_f16_f32 v55, v56, v57
	v_cvt_pk_f16_f32 v56, v50, v51
	v_cndmask_b32_e64 v50, v154, v68, s[4:5]
	v_cvt_pk_f16_f32 v57, v52, v53
	v_lshl_or_b32 v52, v50, 5, v152
	v_pk_mul_f32 v[50:51], v[60:61], v[48:49]
	v_pk_mul_f32 v[46:47], v[146:147], v[46:47]
	v_pk_mul_f32 v[48:49], v[60:61], v[44:45]
	s_and_b64 vcc, exec, s[8:9]
	v_pk_mul_f32 v[44:45], v[146:147], v[42:43]
	global_store_dwordx4 v[58:59], v[54:57], off offset:256 sc0 sc1
	s_cbranch_vccnz .LBB0_411
	v_lshlrev_b32_e32 v42, 2, v52
	global_load_dwordx4 v[54:57], v42, s[12:13]
	global_load_dwordx4 v[58:61], v42, s[12:13] offset:16
	s_waitcnt vmcnt(0)
	v_pk_mul_f32 v[62:63], v[46:47], v[54:55] op_sel:[1,1] op_sel_hi:[1,0]
	v_mul_f32_e32 v64, v51, v57
	v_mul_f32_e32 v66, v51, v56
	v_pk_mul_f32 v[72:73], v[44:45], v[58:59] op_sel:[1,1] op_sel_hi:[1,0]
	v_mul_f32_e32 v74, v49, v61
	v_mul_f32_e32 v76, v49, v60
	v_pk_mul_f32 v[42:43], v[46:47], v[54:55]
	v_pk_mul_f32 v[70:71], v[44:45], v[58:59]
	v_pk_fma_f32 v[46:47], v[46:47], v[54:55], v[62:63] op_sel_hi:[0,1,1]
	v_pk_fma_f32 v[54:55], v[50:51], v[56:57], v[64:65] op_sel_hi:[1,1,0] neg_lo:[0,0,1] neg_hi:[0,0,1]
	v_pk_fma_f32 v[56:57], v[50:51], v[56:57], v[66:67] op_sel:[0,1,0] op_sel_hi:[1,0,0]
	v_pk_fma_f32 v[44:45], v[44:45], v[58:59], v[72:73] op_sel_hi:[0,1,1]
	v_pk_fma_f32 v[50:51], v[48:49], v[60:61], v[74:75] op_sel_hi:[1,1,0] neg_lo:[0,0,1] neg_hi:[0,0,1]
	v_pk_fma_f32 v[58:59], v[48:49], v[60:61], v[76:77] op_sel:[0,1,0] op_sel_hi:[1,0,0]
	v_sub_f32_e32 v44, v70, v72
	v_sub_f32_e32 v46, v42, v62
	v_mov_b32_e32 v48, v50
	v_mov_b32_e32 v49, v58
	v_mov_b32_e32 v50, v54
	v_mov_b32_e32 v51, v56
.LBB0_411:
	v_add_u32_e32 v53, 0x90, v162
	v_mov_b64_e32 v[42:43], s[76:77]
	v_mad_i64_i32 v[42:43], s[2:3], v53, s47, v[42:43]
	v_cvt_pk_f16_f32 v56, v44, v45
	v_mov_b32_e32 v44, v146
	v_mov_b32_e32 v45, v146
	v_lshl_add_u64 v[42:43], v[122:123], 1, v[42:43]
	v_cvt_pk_f16_f32 v54, v46, v47
	v_cvt_pk_f16_f32 v55, v50, v51
	v_cvt_pk_f16_f32 v57, v48, v49
	v_pk_mul_f32 v[40:41], v[44:45], v[40:41]
	v_pk_mul_f32 v[38:39], v[146:147], v[38:39]
	v_pk_mul_f32 v[36:37], v[44:45], v[36:37]
	s_and_b64 vcc, exec, s[8:9]
	v_pk_mul_f32 v[34:35], v[146:147], v[34:35]
	global_store_dwordx4 v[42:43], v[54:57], off sc0 sc1
	s_cbranch_vccnz .LBB0_413
	v_lshlrev_b32_e32 v50, 2, v52
	global_load_dwordx4 v[46:49], v50, s[12:13]
	s_nop 0
	global_load_dwordx4 v[50:53], v50, s[12:13] offset:16
	s_waitcnt vmcnt(0)
	v_pk_mul_f32 v[56:57], v[38:39], v[46:47] op_sel:[1,1] op_sel_hi:[1,0]
	v_mul_f32_e32 v58, v41, v49
	v_mul_f32_e32 v60, v41, v48
	v_pk_mul_f32 v[64:65], v[34:35], v[50:51] op_sel:[1,1] op_sel_hi:[1,0]
	v_mul_f32_e32 v66, v37, v53
	v_mul_f32_e32 v70, v37, v52
	v_pk_mul_f32 v[54:55], v[38:39], v[46:47]
	v_pk_mul_f32 v[62:63], v[34:35], v[50:51]
	v_pk_fma_f32 v[38:39], v[38:39], v[46:47], v[56:57] op_sel_hi:[0,1,1]
	v_pk_fma_f32 v[46:47], v[40:41], v[48:49], v[58:59] op_sel_hi:[1,1,0] neg_lo:[0,0,1] neg_hi:[0,0,1]
	v_pk_fma_f32 v[48:49], v[40:41], v[48:49], v[60:61] op_sel:[0,1,0] op_sel_hi:[1,0,0]
	v_pk_fma_f32 v[34:35], v[34:35], v[50:51], v[64:65] op_sel_hi:[0,1,1]
	v_pk_fma_f32 v[40:41], v[36:37], v[52:53], v[66:67] op_sel_hi:[1,1,0] neg_lo:[0,0,1] neg_hi:[0,0,1]
	v_pk_fma_f32 v[50:51], v[36:37], v[52:53], v[70:71] op_sel:[0,1,0] op_sel_hi:[1,0,0]
	v_sub_f32_e32 v34, v62, v64
	v_sub_f32_e32 v38, v54, v56
	v_mov_b32_e32 v36, v40
	v_mov_b32_e32 v37, v50
	v_mov_b32_e32 v40, v46
	v_mov_b32_e32 v41, v48
.LBB0_413:
	v_cvt_pk_f16_f32 v38, v38, v39
	v_cvt_pk_f16_f32 v39, v40, v41
	v_cvt_pk_f16_f32 v40, v34, v35
	v_cndmask_b32_e64 v34, v155, v68, s[4:5]
	v_cvt_pk_f16_f32 v41, v36, v37
	v_lshl_or_b32 v36, v34, 5, v152
	v_pk_mul_f32 v[34:35], v[44:45], v[32:33]
	v_pk_mul_f32 v[30:31], v[146:147], v[30:31]
	v_pk_mul_f32 v[32:33], v[44:45], v[28:29]
	s_and_b64 vcc, exec, s[8:9]
	v_pk_mul_f32 v[28:29], v[146:147], v[26:27]
	global_store_dwordx4 v[42:43], v[38:41], off offset:256 sc0 sc1
	s_cbranch_vccnz .LBB0_415
	v_lshlrev_b32_e32 v26, 2, v36
	global_load_dwordx4 v[38:41], v26, s[12:13]
	global_load_dwordx4 v[42:45], v26, s[12:13] offset:16
	s_waitcnt vmcnt(0)
	v_pk_mul_f32 v[46:47], v[30:31], v[38:39] op_sel:[1,1] op_sel_hi:[1,0]
	v_mul_f32_e32 v48, v35, v41
	v_mul_f32_e32 v50, v35, v40
	v_pk_mul_f32 v[54:55], v[28:29], v[42:43] op_sel:[1,1] op_sel_hi:[1,0]
	v_mul_f32_e32 v56, v33, v45
	v_mul_f32_e32 v58, v33, v44
	v_pk_mul_f32 v[26:27], v[30:31], v[38:39]
	v_pk_mul_f32 v[52:53], v[28:29], v[42:43]
	v_pk_fma_f32 v[30:31], v[30:31], v[38:39], v[46:47] op_sel_hi:[0,1,1]
	v_pk_fma_f32 v[38:39], v[34:35], v[40:41], v[48:49] op_sel_hi:[1,1,0] neg_lo:[0,0,1] neg_hi:[0,0,1]
	v_pk_fma_f32 v[40:41], v[34:35], v[40:41], v[50:51] op_sel:[0,1,0] op_sel_hi:[1,0,0]
	v_pk_fma_f32 v[28:29], v[28:29], v[42:43], v[54:55] op_sel_hi:[0,1,1]
	v_pk_fma_f32 v[34:35], v[32:33], v[44:45], v[56:57] op_sel_hi:[1,1,0] neg_lo:[0,0,1] neg_hi:[0,0,1]
	v_pk_fma_f32 v[42:43], v[32:33], v[44:45], v[58:59] op_sel:[0,1,0] op_sel_hi:[1,0,0]
	v_sub_f32_e32 v28, v52, v54
	v_sub_f32_e32 v30, v26, v46
	v_mov_b32_e32 v32, v34
	v_mov_b32_e32 v33, v42
	v_mov_b32_e32 v34, v38
	v_mov_b32_e32 v35, v40
;     __device__ __forceinline__ void operator()(const Acc& acc, const Unit& u, int wr, int wc, int fr, int fq) const {
;     ...
;             for (int m = 0; m < 4; ++m) { const int row = row0 + ai * HALF + m * 16; f16* rowp = O + (size_t)row * ZP0 + col0;
;                 const int t = row & (SEQ - 1), prow = t >> 6, pcol = t & 63;
; #pragma unroll
;                 for (int bj = 0; bj < 2; ++bj) { f32x4 v0 = acc[ai][bj][m][0] * sc, v1 = acc[ai][bj][m][1] * sc;
;                     if (dorope) { const int c = col0 + bj * HALF, half = (c >> 5) & 1, i0 = (c & 31) >> 1; const int pos = half ? pcol : prow;
;                         const f32x4* tp = (const f32x4*)(rope + (pos * 16 + i0) * 2); const f32x4 t0 = tp[0], t1 = tp[1];
;                         f32x4 r0, r1;
;                         r0[0] = v0[0] * t0[0] - v0[1] * t0[1]; r0[1] = v0[0] * t0[1] + v0[1] * t0[0];
;                         r0[2] = v0[2] * t0[2] - v0[3] * t0[3]; r0[3] = v0[2] * t0[3] + v0[3] * t0[2];
;                         r1[0] = v1[0] * t1[0] - v1[1] * t1[1]; r1[1] = v1[0] * t1[1] + v1[1] * t1[0];
;                         r1[2] = v1[2] * t1[2] - v1[3] * t1[3]; r1[3] = v1[2] * t1[3] + v1[3] * t1[2];
;                         v0 = r0; v1 = r1; }
;                     u32x4 w; w.x = pkh(v0[0], v0[1]); w.y = pkh(v0[2], v0[3]); w.z = pkh(v1[0], v1[1]); w.w = pkh(v1[2], v1[3]);
;                     *(u32x4*)(rowp + bj * HALF) = w; } }
.LBB0_415:
	v_add_u32_e32 v37, 0xa0, v162
	v_mov_b64_e32 v[26:27], s[76:77]
	v_mad_i64_i32 v[26:27], s[2:3], v37, s47, v[26:27]
	v_cvt_pk_f16_f32 v40, v28, v29
	v_mov_b32_e32 v28, v146
	v_mov_b32_e32 v29, v146
	v_lshl_add_u64 v[26:27], v[122:123], 1, v[26:27]
	v_cvt_pk_f16_f32 v38, v30, v31
	v_cvt_pk_f16_f32 v39, v34, v35
	v_cvt_pk_f16_f32 v41, v32, v33
	v_pk_mul_f32 v[24:25], v[28:29], v[24:25]
	v_pk_mul_f32 v[22:23], v[146:147], v[22:23]
	v_pk_mul_f32 v[20:21], v[28:29], v[20:21]
	s_and_b64 vcc, exec, s[8:9]
	v_pk_mul_f32 v[18:19], v[146:147], v[18:19]
	global_store_dwordx4 v[26:27], v[38:41], off sc0 sc1
	s_cbranch_vccnz .LBB0_417
	v_lshlrev_b32_e32 v34, 2, v36
	global_load_dwordx4 v[30:33], v34, s[12:13]
	s_nop 0
	global_load_dwordx4 v[34:37], v34, s[12:13] offset:16
	s_waitcnt vmcnt(0)
	v_pk_mul_f32 v[40:41], v[22:23], v[30:31] op_sel:[1,1] op_sel_hi:[1,0]
	v_mul_f32_e32 v42, v25, v33
	v_mul_f32_e32 v44, v25, v32
	v_pk_mul_f32 v[48:49], v[18:19], v[34:35] op_sel:[1,1] op_sel_hi:[1,0]
	v_mul_f32_e32 v50, v21, v37
	v_mul_f32_e32 v52, v21, v36
	v_pk_mul_f32 v[38:39], v[22:23], v[30:31]
	v_pk_mul_f32 v[46:47], v[18:19], v[34:35]
	v_pk_fma_f32 v[22:23], v[22:23], v[30:31], v[40:41] op_sel_hi:[0,1,1]
	v_pk_fma_f32 v[30:31], v[24:25], v[32:33], v[42:43] op_sel_hi:[1,1,0] neg_lo:[0,0,1] neg_hi:[0,0,1]
	v_pk_fma_f32 v[32:33], v[24:25], v[32:33], v[44:45] op_sel:[0,1,0] op_sel_hi:[1,0,0]
	v_pk_fma_f32 v[18:19], v[18:19], v[34:35], v[48:49] op_sel_hi:[0,1,1]
	v_pk_fma_f32 v[24:25], v[20:21], v[36:37], v[50:51] op_sel_hi:[1,1,0] neg_lo:[0,0,1] neg_hi:[0,0,1]
	v_pk_fma_f32 v[34:35], v[20:21], v[36:37], v[52:53] op_sel:[0,1,0] op_sel_hi:[1,0,0]
	v_sub_f32_e32 v18, v46, v48
	v_sub_f32_e32 v22, v38, v40
	v_mov_b32_e32 v20, v24
	v_mov_b32_e32 v21, v34
	v_mov_b32_e32 v24, v30
	v_mov_b32_e32 v25, v32
.LBB0_417:
	v_cvt_pk_f16_f32 v22, v22, v23
	v_cvt_pk_f16_f32 v23, v24, v25
	v_cvt_pk_f16_f32 v24, v18, v19
	v_cndmask_b32_e64 v18, v156, v68, s[4:5]
	v_cvt_pk_f16_f32 v25, v20, v21
	v_lshl_or_b32 v20, v18, 5, v152
	v_pk_mul_f32 v[18:19], v[28:29], v[16:17]
	v_pk_mul_f32 v[14:15], v[146:147], v[14:15]
	v_pk_mul_f32 v[16:17], v[28:29], v[12:13]
	s_and_b64 vcc, exec, s[8:9]
	v_pk_mul_f32 v[12:13], v[146:147], v[10:11]
	global_store_dwordx4 v[26:27], v[22:25], off offset:256 sc0 sc1
	s_cbranch_vccnz .LBB0_419
	v_lshlrev_b32_e32 v10, 2, v20
	global_load_dwordx4 v[22:25], v10, s[12:13]
	global_load_dwordx4 v[26:29], v10, s[12:13] offset:16
	s_waitcnt vmcnt(0)
	v_pk_mul_f32 v[30:31], v[14:15], v[22:23] op_sel:[1,1] op_sel_hi:[1,0]
	v_mul_f32_e32 v32, v19, v25
	v_mul_f32_e32 v34, v19, v24
	v_pk_mul_f32 v[38:39], v[12:13], v[26:27] op_sel:[1,1] op_sel_hi:[1,0]
	v_mul_f32_e32 v40, v17, v29
	v_mul_f32_e32 v42, v17, v28
	v_pk_mul_f32 v[10:11], v[14:15], v[22:23]
	v_pk_mul_f32 v[36:37], v[12:13], v[26:27]
	v_pk_fma_f32 v[14:15], v[14:15], v[22:23], v[30:31] op_sel_hi:[0,1,1]
	v_pk_fma_f32 v[22:23], v[18:19], v[24:25], v[32:33] op_sel_hi:[1,1,0] neg_lo:[0,0,1] neg_hi:[0,0,1]
	v_pk_fma_f32 v[24:25], v[18:19], v[24:25], v[34:35] op_sel:[0,1,0] op_sel_hi:[1,0,0]
	v_pk_fma_f32 v[12:13], v[12:13], v[26:27], v[38:39] op_sel_hi:[0,1,1]
	v_pk_fma_f32 v[18:19], v[16:17], v[28:29], v[40:41] op_sel_hi:[1,1,0] neg_lo:[0,0,1] neg_hi:[0,0,1]
	v_pk_fma_f32 v[26:27], v[16:17], v[28:29], v[42:43] op_sel:[0,1,0] op_sel_hi:[1,0,0]
	v_sub_f32_e32 v12, v36, v38
	v_sub_f32_e32 v14, v10, v30
	v_mov_b32_e32 v16, v18
	v_mov_b32_e32 v17, v26
	v_mov_b32_e32 v18, v22
	v_mov_b32_e32 v19, v24
.LBB0_419:
	v_add_u32_e32 v21, 0xb0, v162
	v_mov_b64_e32 v[10:11], s[76:77]
	v_mad_i64_i32 v[10:11], s[2:3], v21, s47, v[10:11]
	v_cvt_pk_f16_f32 v24, v12, v13
	v_mov_b32_e32 v12, v146
	v_mov_b32_e32 v13, v146
	v_lshl_add_u64 v[10:11], v[122:123], 1, v[10:11]
	v_cvt_pk_f16_f32 v22, v14, v15
	v_cvt_pk_f16_f32 v23, v18, v19
	v_cvt_pk_f16_f32 v25, v16, v17
	v_pk_mul_f32 v[8:9], v[12:13], v[8:9]
	v_pk_mul_f32 v[6:7], v[146:147], v[6:7]
	v_pk_mul_f32 v[4:5], v[12:13], v[4:5]
	s_and_b64 vcc, exec, s[8:9]
	v_pk_mul_f32 v[2:3], v[146:147], v[2:3]
	global_store_dwordx4 v[10:11], v[22:25], off sc0 sc1
	s_cbranch_vccnz .LBB0_421
	v_lshlrev_b32_e32 v16, 2, v20
	global_load_dwordx4 v[12:15], v16, s[12:13]
	s_nop 0
	global_load_dwordx4 v[16:19], v16, s[12:13] offset:16
	s_waitcnt vmcnt(0)
	v_pk_mul_f32 v[22:23], v[6:7], v[12:13] op_sel:[1,1] op_sel_hi:[1,0]
	v_mul_f32_e32 v24, v9, v15
	v_mul_f32_e32 v26, v9, v14
	v_pk_mul_f32 v[30:31], v[2:3], v[16:17] op_sel:[1,1] op_sel_hi:[1,0]
	v_mul_f32_e32 v32, v5, v19
	v_mul_f32_e32 v34, v5, v18
	v_pk_mul_f32 v[20:21], v[6:7], v[12:13]
	v_pk_mul_f32 v[28:29], v[2:3], v[16:17]
	v_pk_fma_f32 v[6:7], v[6:7], v[12:13], v[22:23] op_sel_hi:[0,1,1]
	v_pk_fma_f32 v[12:13], v[8:9], v[14:15], v[24:25] op_sel_hi:[1,1,0] neg_lo:[0,0,1] neg_hi:[0,0,1]
	v_pk_fma_f32 v[14:15], v[8:9], v[14:15], v[26:27] op_sel:[0,1,0] op_sel_hi:[1,0,0]
	v_pk_fma_f32 v[2:3], v[2:3], v[16:17], v[30:31] op_sel_hi:[0,1,1]
	v_pk_fma_f32 v[8:9], v[4:5], v[18:19], v[32:33] op_sel_hi:[1,1,0] neg_lo:[0,0,1] neg_hi:[0,0,1]
	v_pk_fma_f32 v[16:17], v[4:5], v[18:19], v[34:35] op_sel:[0,1,0] op_sel_hi:[1,0,0]
	v_sub_f32_e32 v2, v28, v30
	v_sub_f32_e32 v6, v20, v22
	v_mov_b32_e32 v4, v8
	v_mov_b32_e32 v5, v16
	v_mov_b32_e32 v8, v12
	v_mov_b32_e32 v9, v14
.LBB0_421:
	v_cvt_pk_f16_f32 v6, v6, v7
	v_cvt_pk_f16_f32 v7, v8, v9
	v_cvt_pk_f16_f32 v8, v2, v3
	v_cvt_pk_f16_f32 v9, v4, v5
	s_andn2_b64 vcc, exec, s[6:7]
	s_mov_b64 s[2:3], -1
	global_store_dwordx4 v[10:11], v[6:9], off offset:256 sc0 sc1
	s_cbranch_vccnz .LBB0_376
	s_andn2_b64 vcc, exec, s[10:11]
	s_cbranch_vccnz .LBB0_375
	s_barrier
	s_branch .LBB0_375

;     __device__ __forceinline__ void operator()(const Acc& acc, const Unit& u, int wr, int wc, int fr, int fq) const {
;     ...
;             for (int m = 0; m < 4; ++m) { const int row = row0 + ai * HALF + m * 16; const float s = gv[((row >> 8) * NE + u.g) * CAP + (row & 255)];
;                 f16* rowp = Og + (size_t)row * DM + col0;
; #pragma unroll
;                 for (int bj = 0; bj < 2; ++bj) { const f32x4 v0 = acc[ai][bj][m][0] * s, v1 = acc[ai][bj][m][1] * s;
;                     u32x4 w; w.x = pkh(v0[0], v0[1]); w.y = pkh(v0[2], v0[3]); w.z = pkh(v1[0], v1[1]); w.w = pkh(v1[2], v1[3]);
;                     *(u32x4*)(rowp + bj * HALF) = w; } }
.LBB0_1105:
	v_lshl_add_u32 v148, s48, 8, v1
	v_lshrrev_b32_e32 v146, 4, v148
	v_and_b32_e32 v146, 0xfffff0, v146
	v_add_lshl_u32 v166, v146, s18, 8
	v_or_b32_e32 v146, v166, v151
	v_ashrrev_i32_e32 v147, 31, v146
	v_lshl_add_u64 v[146:147], v[146:147], 2, s[72:73]
	global_load_dword v156, v[146:147], off
	v_lshl_or_b32 v146, s19, 8, v152
	s_ashr_i32 s19, s18, 31
	s_lshl_b64 s[2:3], s[18:19], 23
	s_add_u32 s2, s74, s2
	v_ashrrev_i32_e32 v147, 31, v146
	v_ashrrev_i32_e32 v149, 31, v148
	v_or_b32_e32 v158, 16, v148
	s_addc_u32 s3, s75, s3
	v_lshlrev_b64 v[160:161], 11, v[148:149]
	v_lshl_add_u64 v[146:147], v[146:147], 1, s[2:3]
	v_and_or_b32 v162, v158, s44, v166
	v_lshl_add_u64 v[160:161], v[146:147], 0, v[160:161]
	v_ashrrev_i32_e32 v163, 31, v162
	v_lshl_add_u64 v[162:163], v[162:163], 2, s[72:73]
	v_ashrrev_i32_e32 v159, 31, v158
	s_movk_i32 s2, 0xcf
	s_and_b64 vcc, exec, s[4:5]
	s_waitcnt vmcnt(0)
	v_pk_mul_f32 v[128:129], v[128:129], v[156:157] op_sel_hi:[1,0]
	v_pk_mul_f32 v[126:127], v[126:127], v[156:157] op_sel_hi:[1,0]
	v_pk_mul_f32 v[124:125], v[124:125], v[156:157] op_sel_hi:[1,0]
	v_pk_mul_f32 v[122:123], v[122:123], v[156:157] op_sel_hi:[1,0]
	v_pk_mul_f32 v[120:121], v[120:121], v[156:157] op_sel_hi:[1,0]
	v_pk_mul_f32 v[118:119], v[118:119], v[156:157] op_sel_hi:[1,0]
	v_pk_mul_f32 v[164:165], v[116:117], v[156:157] op_sel_hi:[1,0]
	v_pk_mul_f32 v[156:157], v[114:115], v[156:157] op_sel_hi:[1,0]
	v_cvt_pk_f16_f32 v114, v126, v127
	v_cvt_pk_f16_f32 v115, v128, v129
	v_cvt_pk_f16_f32 v116, v122, v123
	v_cvt_pk_f16_f32 v117, v124, v125
	v_cvt_pk_f16_f32 v118, v118, v119
	v_cvt_pk_f16_f32 v119, v120, v121
	v_cvt_pk_f16_f32 v120, v156, v157
	v_cvt_pk_f16_f32 v121, v164, v165
	global_store_dwordx4 v[160:161], v[114:117], off sc0 sc1
	global_store_dwordx4 v[160:161], v[118:121], off offset:256 sc0 sc1
	global_load_dword v114, v[162:163], off
	v_or_b32_e32 v116, 32, v148
	v_lshlrev_b64 v[118:119], 11, v[158:159]
	v_and_or_b32 v120, v116, s45, v166
	v_lshl_add_u64 v[118:119], v[146:147], 0, v[118:119]
	v_ashrrev_i32_e32 v121, 31, v120
	v_lshl_add_u64 v[120:121], v[120:121], 2, s[72:73]
	v_ashrrev_i32_e32 v117, 31, v116
	s_waitcnt vmcnt(0)
	v_pk_mul_f32 v[112:113], v[112:113], v[114:115] op_sel_hi:[1,0]
	v_pk_mul_f32 v[110:111], v[110:111], v[114:115] op_sel_hi:[1,0]
	v_pk_mul_f32 v[108:109], v[108:109], v[114:115] op_sel_hi:[1,0]
	v_pk_mul_f32 v[106:107], v[106:107], v[114:115] op_sel_hi:[1,0]
	v_pk_mul_f32 v[104:105], v[104:105], v[114:115] op_sel_hi:[1,0]
	v_pk_mul_f32 v[102:103], v[102:103], v[114:115] op_sel_hi:[1,0]
	v_pk_mul_f32 v[122:123], v[100:101], v[114:115] op_sel_hi:[1,0]
	v_pk_mul_f32 v[114:115], v[98:99], v[114:115] op_sel_hi:[1,0]
	v_cvt_pk_f16_f32 v98, v110, v111
	v_cvt_pk_f16_f32 v99, v112, v113
	v_cvt_pk_f16_f32 v100, v106, v107
	v_cvt_pk_f16_f32 v101, v108, v109
	v_cvt_pk_f16_f32 v102, v102, v103
	v_cvt_pk_f16_f32 v103, v104, v105
	v_cvt_pk_f16_f32 v104, v114, v115
	v_cvt_pk_f16_f32 v105, v122, v123
	global_store_dwordx4 v[118:119], v[98:101], off sc0 sc1
	global_store_dwordx4 v[118:119], v[102:105], off offset:256 sc0 sc1
	global_load_dword v98, v[120:121], off
	v_or_b32_e32 v100, 48, v148
	v_lshlrev_b64 v[102:103], 11, v[116:117]
	v_and_or_b32 v104, v100, s46, v166
	v_lshl_add_u64 v[102:103], v[146:147], 0, v[102:103]
	v_ashrrev_i32_e32 v105, 31, v104
	v_lshl_add_u64 v[104:105], v[104:105], 2, s[72:73]
	v_ashrrev_i32_e32 v101, 31, v100
	s_waitcnt vmcnt(0)
	v_pk_mul_f32 v[96:97], v[96:97], v[98:99] op_sel_hi:[1,0]
	v_pk_mul_f32 v[94:95], v[94:95], v[98:99] op_sel_hi:[1,0]
	v_pk_mul_f32 v[92:93], v[92:93], v[98:99] op_sel_hi:[1,0]
	v_pk_mul_f32 v[90:91], v[90:91], v[98:99] op_sel_hi:[1,0]
	v_pk_mul_f32 v[88:89], v[88:89], v[98:99] op_sel_hi:[1,0]
	v_pk_mul_f32 v[86:87], v[86:87], v[98:99] op_sel_hi:[1,0]
	v_pk_mul_f32 v[106:107], v[84:85], v[98:99] op_sel_hi:[1,0]
	v_pk_mul_f32 v[98:99], v[82:83], v[98:99] op_sel_hi:[1,0]
	v_cvt_pk_f16_f32 v82, v94, v95
	v_cvt_pk_f16_f32 v83, v96, v97
	v_cvt_pk_f16_f32 v84, v90, v91
	v_cvt_pk_f16_f32 v85, v92, v93
	v_cvt_pk_f16_f32 v86, v86, v87
	v_cvt_pk_f16_f32 v87, v88, v89
	v_cvt_pk_f16_f32 v88, v98, v99
	v_cvt_pk_f16_f32 v89, v106, v107
	global_store_dwordx4 v[102:103], v[82:85], off sc0 sc1
	global_store_dwordx4 v[102:103], v[86:89], off offset:256 sc0 sc1
	global_load_dword v82, v[104:105], off
	v_add_u32_e32 v84, 0x80, v148
	v_lshrrev_b32_e32 v83, 4, v84
	v_and_b32_e32 v83, 0xfffff0, v83
	v_add_lshl_u32 v92, v83, s18, 8
	v_lshlrev_b64 v[86:87], 11, v[100:101]
	v_and_or_b32 v88, v84, s2, v92
	v_lshl_add_u64 v[86:87], v[146:147], 0, v[86:87]
	v_ashrrev_i32_e32 v89, 31, v88
	v_lshl_add_u64 v[88:89], v[88:89], 2, s[72:73]
	v_ashrrev_i32_e32 v85, 31, v84
	s_mov_b64 s[2:3], -1
	s_waitcnt vmcnt(0)
;     __device__ __forceinline__ void operator()(const Acc& acc, const Unit& u, int wr, int wc, int fr, int fq) const {
;     ...
;             for (int m = 0; m < 4; ++m) { const int row = row0 + ai * HALF + m * 16; const float s = gv[((row >> 8) * NE + u.g) * CAP + (row & 255)];
;                 f16* rowp = Og + (size_t)row * DM + col0;
; #pragma unroll
;                 for (int bj = 0; bj < 2; ++bj) { const f32x4 v0 = acc[ai][bj][m][0] * s, v1 = acc[ai][bj][m][1] * s;
;                     u32x4 w; w.x = pkh(v0[0], v0[1]); w.y = pkh(v0[2], v0[3]); w.z = pkh(v1[0], v1[1]); w.w = pkh(v1[2], v1[3]);
;                     *(u32x4*)(rowp + bj * HALF) = w; } }
	v_pk_mul_f32 v[80:81], v[80:81], v[82:83] op_sel_hi:[1,0]
	v_pk_mul_f32 v[78:79], v[78:79], v[82:83] op_sel_hi:[1,0]
	v_pk_mul_f32 v[76:77], v[76:77], v[82:83] op_sel_hi:[1,0]
	v_pk_mul_f32 v[74:75], v[74:75], v[82:83] op_sel_hi:[1,0]
	v_pk_mul_f32 v[72:73], v[72:73], v[82:83] op_sel_hi:[1,0]
	v_pk_mul_f32 v[70:71], v[70:71], v[82:83] op_sel_hi:[1,0]
	v_pk_mul_f32 v[90:91], v[68:69], v[82:83] op_sel_hi:[1,0]
	v_pk_mul_f32 v[82:83], v[66:67], v[82:83] op_sel_hi:[1,0]
	v_cvt_pk_f16_f32 v66, v78, v79
	v_cvt_pk_f16_f32 v67, v80, v81
	v_cvt_pk_f16_f32 v68, v74, v75
	v_cvt_pk_f16_f32 v69, v76, v77
	v_cvt_pk_f16_f32 v70, v70, v71
	v_cvt_pk_f16_f32 v71, v72, v73
	v_cvt_pk_f16_f32 v72, v82, v83
	v_cvt_pk_f16_f32 v73, v90, v91
	global_store_dwordx4 v[86:87], v[66:69], off sc0 sc1
	global_store_dwordx4 v[86:87], v[70:73], off offset:256 sc0 sc1
	global_load_dword v66, v[88:89], off
	v_add_u32_e32 v68, 0x90, v148
	v_lshlrev_b64 v[70:71], 11, v[84:85]
	v_and_or_b32 v72, v68, s44, v92
	v_lshl_add_u64 v[70:71], v[146:147], 0, v[70:71]
	v_ashrrev_i32_e32 v73, 31, v72
	v_lshl_add_u64 v[72:73], v[72:73], 2, s[72:73]
	v_ashrrev_i32_e32 v69, 31, v68
	s_waitcnt vmcnt(0)
	v_pk_mul_f32 v[64:65], v[64:65], v[66:67] op_sel_hi:[1,0]
	v_pk_mul_f32 v[62:63], v[62:63], v[66:67] op_sel_hi:[1,0]
	v_pk_mul_f32 v[60:61], v[60:61], v[66:67] op_sel_hi:[1,0]
	v_pk_mul_f32 v[58:59], v[58:59], v[66:67] op_sel_hi:[1,0]
	v_pk_mul_f32 v[56:57], v[56:57], v[66:67] op_sel_hi:[1,0]
	v_pk_mul_f32 v[54:55], v[54:55], v[66:67] op_sel_hi:[1,0]
	v_pk_mul_f32 v[74:75], v[52:53], v[66:67] op_sel_hi:[1,0]
	v_pk_mul_f32 v[66:67], v[50:51], v[66:67] op_sel_hi:[1,0]
	v_cvt_pk_f16_f32 v50, v62, v63
	v_cvt_pk_f16_f32 v51, v64, v65
	v_cvt_pk_f16_f32 v52, v58, v59
	v_cvt_pk_f16_f32 v53, v60, v61
	v_cvt_pk_f16_f32 v54, v54, v55
	v_cvt_pk_f16_f32 v55, v56, v57
	v_cvt_pk_f16_f32 v56, v66, v67
	v_cvt_pk_f16_f32 v57, v74, v75
	global_store_dwordx4 v[70:71], v[50:53], off sc0 sc1
	global_store_dwordx4 v[70:71], v[54:57], off offset:256 sc0 sc1
	global_load_dword v50, v[72:73], off
	v_add_u32_e32 v52, 0xa0, v148
	v_lshlrev_b64 v[54:55], 11, v[68:69]
	v_and_or_b32 v56, v52, s45, v92
	v_lshl_add_u64 v[54:55], v[146:147], 0, v[54:55]
	v_ashrrev_i32_e32 v57, 31, v56
	v_lshl_add_u64 v[56:57], v[56:57], 2, s[72:73]
	v_ashrrev_i32_e32 v53, 31, v52
	s_waitcnt vmcnt(0)
	v_pk_mul_f32 v[48:49], v[48:49], v[50:51] op_sel_hi:[1,0]
	v_pk_mul_f32 v[46:47], v[46:47], v[50:51] op_sel_hi:[1,0]
	v_pk_mul_f32 v[44:45], v[44:45], v[50:51] op_sel_hi:[1,0]
	v_pk_mul_f32 v[42:43], v[42:43], v[50:51] op_sel_hi:[1,0]
	v_pk_mul_f32 v[40:41], v[40:41], v[50:51] op_sel_hi:[1,0]
	v_pk_mul_f32 v[38:39], v[38:39], v[50:51] op_sel_hi:[1,0]
	v_pk_mul_f32 v[58:59], v[36:37], v[50:51] op_sel_hi:[1,0]
	v_pk_mul_f32 v[50:51], v[34:35], v[50:51] op_sel_hi:[1,0]
	v_cvt_pk_f16_f32 v34, v46, v47
	v_cvt_pk_f16_f32 v35, v48, v49
	v_cvt_pk_f16_f32 v36, v42, v43
	v_cvt_pk_f16_f32 v37, v44, v45
	v_cvt_pk_f16_f32 v38, v38, v39
	v_cvt_pk_f16_f32 v39, v40, v41
	v_cvt_pk_f16_f32 v40, v50, v51
	v_cvt_pk_f16_f32 v41, v58, v59
	global_store_dwordx4 v[54:55], v[34:37], off sc0 sc1
	global_store_dwordx4 v[54:55], v[38:41], off offset:256 sc0 sc1
	global_load_dword v34, v[56:57], off
	v_add_u32_e32 v36, 0xb0, v148
	v_lshlrev_b64 v[38:39], 11, v[52:53]
	v_and_or_b32 v40, v36, s46, v92
	v_lshl_add_u64 v[38:39], v[146:147], 0, v[38:39]
	v_ashrrev_i32_e32 v41, 31, v40
	v_lshl_add_u64 v[40:41], v[40:41], 2, s[72:73]
	v_ashrrev_i32_e32 v37, 31, v36
	s_waitcnt vmcnt(0)
	v_pk_mul_f32 v[32:33], v[32:33], v[34:35] op_sel_hi:[1,0]
	v_pk_mul_f32 v[30:31], v[30:31], v[34:35] op_sel_hi:[1,0]
	v_pk_mul_f32 v[28:29], v[28:29], v[34:35] op_sel_hi:[1,0]
	v_pk_mul_f32 v[26:27], v[26:27], v[34:35] op_sel_hi:[1,0]
	v_pk_mul_f32 v[24:25], v[24:25], v[34:35] op_sel_hi:[1,0]
	v_pk_mul_f32 v[22:23], v[22:23], v[34:35] op_sel_hi:[1,0]
	v_pk_mul_f32 v[42:43], v[20:21], v[34:35] op_sel_hi:[1,0]
	v_pk_mul_f32 v[34:35], v[18:19], v[34:35] op_sel_hi:[1,0]
	v_cvt_pk_f16_f32 v18, v30, v31
	v_cvt_pk_f16_f32 v19, v32, v33
	v_cvt_pk_f16_f32 v20, v26, v27
	v_cvt_pk_f16_f32 v21, v28, v29
	v_cvt_pk_f16_f32 v22, v22, v23
	v_cvt_pk_f16_f32 v23, v24, v25
	v_cvt_pk_f16_f32 v24, v34, v35
	v_cvt_pk_f16_f32 v25, v42, v43
	global_store_dwordx4 v[38:39], v[18:21], off sc0 sc1
	global_store_dwordx4 v[38:39], v[22:25], off offset:256 sc0 sc1
	global_load_dword v18, v[40:41], off
	v_lshlrev_b64 v[20:21], 11, v[36:37]
	v_lshl_add_u64 v[20:21], v[146:147], 0, v[20:21]
	s_waitcnt vmcnt(0)
	v_pk_mul_f32 v[16:17], v[16:17], v[18:19] op_sel_hi:[1,0]
	v_pk_mul_f32 v[14:15], v[14:15], v[18:19] op_sel_hi:[1,0]
	v_pk_mul_f32 v[12:13], v[12:13], v[18:19] op_sel_hi:[1,0]
	v_pk_mul_f32 v[10:11], v[10:11], v[18:19] op_sel_hi:[1,0]
	v_pk_mul_f32 v[8:9], v[8:9], v[18:19] op_sel_hi:[1,0]
	v_pk_mul_f32 v[6:7], v[6:7], v[18:19] op_sel_hi:[1,0]
	v_pk_mul_f32 v[22:23], v[4:5], v[18:19] op_sel_hi:[1,0]
	v_pk_mul_f32 v[18:19], v[2:3], v[18:19] op_sel_hi:[1,0]
	v_cvt_pk_f16_f32 v2, v14, v15
	v_cvt_pk_f16_f32 v3, v16, v17
	v_cvt_pk_f16_f32 v4, v10, v11
	v_cvt_pk_f16_f32 v5, v12, v13
	v_cvt_pk_f16_f32 v6, v6, v7
	v_cvt_pk_f16_f32 v7, v8, v9
	v_cvt_pk_f16_f32 v8, v18, v19
	v_cvt_pk_f16_f32 v9, v22, v23
	global_store_dwordx4 v[20:21], v[2:5], off sc0 sc1
	global_store_dwordx4 v[20:21], v[6:9], off offset:256 sc0 sc1
	s_cbranch_vccnz .LBB0_1087
	s_andn2_b64 vcc, exec, s[10:11]
	s_cbranch_vccnz .LBB0_1086
	s_barrier
	s_branch .LBB0_1086

;     __device__ __forceinline__ void operator()(const Acc& acc, const Unit& u, int wr, int wc, int fr, int fq) const {
;     ...
;         } else {
;             const int col0 = 1024 + (u.pn - 8) * BM + wc * 32 + 8 * fq;
; #pragma unroll
;             for (int ai = 0; ai < 2; ++ai)
; #pragma unroll
;                 for (int m = 0; m < 4; ++m) { f16* rowp = O + (size_t)(row0 + ai * HALF + m * 16) * ZP1N + col0;
; #pragma unroll
;                     for (int bj = 0; bj < 2; ++bj) { const f32x4 v0 = acc[ai][bj][m][0], v1 = acc[ai][bj][m][1];
;                         u32x4 w; w.x = pkh(v0[0], v0[1]); w.y = pkh(v0[2], v0[3]); w.z = pkh(v1[0], v1[1]); w.w = pkh(v1[2], v1[3]);
;                         *(u32x4*)(rowp + bj * HALF) = w; } }
.LBB0_1287:
	v_lshl_add_u32 v138, s43, 8, v150
	v_mov_b64_e32 v[160:161], s[76:77]
	v_mad_i64_i32 v[156:157], s[2:3], v154, s42, v[160:161]
	v_lshlrev_b64 v[162:163], 1, v[138:139]
	v_lshl_add_u64 v[164:165], v[156:157], 0, v[162:163]
	v_cvt_pk_f16_f32 v156, v126, v127
	v_cvt_pk_f16_f32 v157, v128, v129
	v_cvt_pk_f16_f32 v158, v118, v119
	v_cvt_pk_f16_f32 v159, v120, v121
	global_store_dwordx4 v[164:165], v[156:159], off sc0 sc1
	v_or_b32_e32 v138, 16, v154
	s_nop 0
	v_cvt_pk_f16_f32 v156, v122, v123
	v_cvt_pk_f16_f32 v157, v124, v125
	v_cvt_pk_f16_f32 v158, v114, v115
	v_cvt_pk_f16_f32 v159, v116, v117
	global_store_dwordx4 v[164:165], v[156:159], off offset:256 sc0 sc1
	s_nop 1
	v_mad_i64_i32 v[156:157], s[2:3], v138, s42, v[160:161]
	v_lshl_add_u64 v[164:165], v[156:157], 0, v[162:163]
	v_cvt_pk_f16_f32 v156, v110, v111
	v_cvt_pk_f16_f32 v157, v112, v113
	v_cvt_pk_f16_f32 v158, v102, v103
	v_cvt_pk_f16_f32 v159, v104, v105
	global_store_dwordx4 v[164:165], v[156:159], off sc0 sc1
	v_or_b32_e32 v138, 32, v154
	s_nop 0
	v_cvt_pk_f16_f32 v156, v106, v107
	v_cvt_pk_f16_f32 v157, v108, v109
	v_cvt_pk_f16_f32 v158, v98, v99
	v_cvt_pk_f16_f32 v159, v100, v101
	global_store_dwordx4 v[164:165], v[156:159], off offset:256 sc0 sc1
	s_nop 1
	v_mad_i64_i32 v[156:157], s[2:3], v138, s42, v[160:161]
	v_lshl_add_u64 v[164:165], v[156:157], 0, v[162:163]
	v_cvt_pk_f16_f32 v156, v94, v95
	v_cvt_pk_f16_f32 v157, v96, v97
	v_cvt_pk_f16_f32 v158, v86, v87
	v_cvt_pk_f16_f32 v159, v88, v89
	global_store_dwordx4 v[164:165], v[156:159], off sc0 sc1
	v_or_b32_e32 v138, 48, v154
	s_nop 0
	v_cvt_pk_f16_f32 v156, v90, v91
	v_cvt_pk_f16_f32 v157, v92, v93
	v_cvt_pk_f16_f32 v158, v82, v83
	v_cvt_pk_f16_f32 v159, v84, v85
	global_store_dwordx4 v[164:165], v[156:159], off offset:256 sc0 sc1
	s_nop 1
	v_mad_i64_i32 v[156:157], s[2:3], v138, s42, v[160:161]
	v_lshl_add_u64 v[164:165], v[156:157], 0, v[162:163]
	v_cvt_pk_f16_f32 v156, v78, v79
	v_cvt_pk_f16_f32 v157, v80, v81
	v_cvt_pk_f16_f32 v158, v70, v71
	v_cvt_pk_f16_f32 v159, v72, v73
	global_store_dwordx4 v[164:165], v[156:159], off sc0 sc1
	v_add_u32_e32 v138, 0x80, v154
	s_nop 0
	v_cvt_pk_f16_f32 v156, v74, v75
	v_cvt_pk_f16_f32 v157, v76, v77
	v_cvt_pk_f16_f32 v158, v66, v67
	v_cvt_pk_f16_f32 v159, v68, v69
	global_store_dwordx4 v[164:165], v[156:159], off offset:256 sc0 sc1
	s_nop 1
	v_mad_i64_i32 v[156:157], s[2:3], v138, s42, v[160:161]
	v_lshl_add_u64 v[164:165], v[156:157], 0, v[162:163]
	v_cvt_pk_f16_f32 v156, v62, v63
	v_cvt_pk_f16_f32 v157, v64, v65
	v_cvt_pk_f16_f32 v158, v54, v55
	v_cvt_pk_f16_f32 v159, v56, v57
	global_store_dwordx4 v[164:165], v[156:159], off sc0 sc1
	v_add_u32_e32 v138, 0x90, v154
	s_nop 0
	v_cvt_pk_f16_f32 v156, v58, v59
	v_cvt_pk_f16_f32 v157, v60, v61
	v_cvt_pk_f16_f32 v158, v50, v51
	v_cvt_pk_f16_f32 v159, v52, v53
	global_store_dwordx4 v[164:165], v[156:159], off offset:256 sc0 sc1
	s_nop 1
	v_mad_i64_i32 v[156:157], s[2:3], v138, s42, v[160:161]
	v_lshl_add_u64 v[164:165], v[156:157], 0, v[162:163]
	v_cvt_pk_f16_f32 v156, v46, v47
	v_cvt_pk_f16_f32 v157, v48, v49
	v_cvt_pk_f16_f32 v158, v38, v39
	v_cvt_pk_f16_f32 v159, v40, v41
	global_store_dwordx4 v[164:165], v[156:159], off sc0 sc1
	v_add_u32_e32 v138, 0xa0, v154
	s_nop 0
	v_cvt_pk_f16_f32 v156, v42, v43
	v_cvt_pk_f16_f32 v157, v44, v45
	v_cvt_pk_f16_f32 v158, v34, v35
	v_cvt_pk_f16_f32 v159, v36, v37
	global_store_dwordx4 v[164:165], v[156:159], off offset:256 sc0 sc1
	s_nop 1
	v_mad_i64_i32 v[156:157], s[2:3], v138, s42, v[160:161]
	v_lshl_add_u64 v[164:165], v[156:157], 0, v[162:163]
	v_cvt_pk_f16_f32 v156, v30, v31
	v_cvt_pk_f16_f32 v157, v32, v33
	v_cvt_pk_f16_f32 v158, v22, v23
	v_cvt_pk_f16_f32 v159, v24, v25
	global_store_dwordx4 v[164:165], v[156:159], off sc0 sc1
	v_add_u32_e32 v138, 0xb0, v154
	s_nop 0
	v_cvt_pk_f16_f32 v156, v26, v27
	v_cvt_pk_f16_f32 v157, v28, v29
	v_cvt_pk_f16_f32 v158, v18, v19
	v_cvt_pk_f16_f32 v159, v20, v21
	global_store_dwordx4 v[164:165], v[156:159], off offset:256 sc0 sc1
	s_nop 1
	v_mad_i64_i32 v[156:157], s[2:3], v138, s42, v[160:161]
	v_lshl_add_u64 v[160:161], v[156:157], 0, v[162:163]
	v_cvt_pk_f16_f32 v156, v14, v15
	v_cvt_pk_f16_f32 v157, v16, v17
	v_cvt_pk_f16_f32 v158, v6, v7
	v_cvt_pk_f16_f32 v159, v8, v9
	global_store_dwordx4 v[160:161], v[156:159], off sc0 sc1
	s_nop 1
	v_cvt_pk_f16_f32 v156, v10, v11
	v_cvt_pk_f16_f32 v157, v12, v13
	v_cvt_pk_f16_f32 v158, v2, v3
	v_cvt_pk_f16_f32 v159, v4, v5
	global_store_dwordx4 v[160:161], v[156:159], off offset:256 sc0 sc1
	s_cbranch_execnz .LBB0_1285
;     __device__ __forceinline__ void operator()(const Acc& acc, const Unit& u, int wr, int wc, int fr, int fq) const {
;     ...
;         if (u.pn < 8) {
;             const int col0 = (u.pn < 4 ? 0 : 512) + 128 * (u.pn & 3) + wc * 32 + 8 * fq; const bool glu = u.pn >= 4;
; #pragma unroll
;             for (int ai = 0; ai < 2; ++ai)
; #pragma unroll
;                 for (int m = 0; m < 4; ++m) { float h[8];
; #pragma unroll
;                     for (int n = 0; n < 2; ++n)
; #pragma unroll
;                         for (int j = 0; j < 4; ++j) { const float a = acc[ai][0][m][n][j], b = acc[ai][1][m][n][j]; h[n * 4 + j] = glu ? a * __builtin_amdgcn_rcpf(1.f + __builtin_amdgcn_exp2f(-LOG2E * b)) : a * b; }
;                     u32x4 w; w.x = pkh(h[0], h[1]); w.y = pkh(h[2], h[3]); w.z = pkh(h[4], h[5]); w.w = pkh(h[6], h[7]);
;                     *(u32x4*)(O + (size_t)(row0 + ai * HALF + m * 16) * ZP1N + col0) = w; }
.LBB0_1288:
	v_mul_f32_e32 v155, 0xbfb8aa3b, v122
	v_exp_f32_e32 v155, v155
	s_cmp_lt_i32 s43, 4
	s_cselect_b32 s2, 0, 0x200
	s_lshl_b32 s3, s43, 7
	v_mul_f32_e32 v156, 0xbfb8aa3b, v123
	v_add_f32_e32 v155, 1.0, v155
	s_and_b32 s3, s3, 0x180
	v_exp_f32_e32 v156, v156
	v_rcp_f32_e32 v155, v155
	s_or_b32 s2, s3, s2
	s_cmp_gt_i32 s43, 3
	s_cselect_b64 vcc, -1, 0
	v_add_f32_e32 v156, 1.0, v156
	v_cndmask_b32_e32 v122, v122, v155, vcc
	v_rcp_f32_e32 v156, v156
	v_mul_f32_e32 v122, v126, v122
	v_mul_f32_e32 v126, 0xbfb8aa3b, v124
	v_mul_f32_e32 v155, 0xbfb8aa3b, v125
	v_exp_f32_e32 v126, v126
	v_exp_f32_e32 v155, v155
	v_cndmask_b32_e32 v123, v123, v156, vcc
	v_mul_f32_e32 v123, v127, v123
	v_add_f32_e32 v126, 1.0, v126
	v_add_f32_e32 v127, 1.0, v155
	v_mul_f32_e32 v155, 0xbfb8aa3b, v114
	v_rcp_f32_e32 v126, v126
	v_exp_f32_e32 v155, v155
	v_rcp_f32_e32 v127, v127
	v_or_b32_e32 v138, s2, v149
	v_cndmask_b32_e32 v124, v124, v126, vcc
	v_add_f32_e32 v126, 1.0, v155
	v_cndmask_b32_e32 v125, v125, v127, vcc
	v_rcp_f32_e32 v126, v126
	v_mul_f32_e32 v127, 0xbfb8aa3b, v115
	v_exp_f32_e32 v127, v127
	v_mul_f32_e32 v124, v128, v124
	v_cndmask_b32_e32 v114, v114, v126, vcc
	v_mul_f32_e32 v114, v118, v114
	v_add_f32_e32 v118, 1.0, v127
	v_mul_f32_e32 v126, 0xbfb8aa3b, v116
	v_rcp_f32_e32 v118, v118
	v_exp_f32_e32 v126, v126
	v_mul_f32_e32 v127, 0xbfb8aa3b, v117
	v_exp_f32_e32 v127, v127
	v_cndmask_b32_e32 v115, v115, v118, vcc
	v_add_f32_e32 v118, 1.0, v126
	v_rcp_f32_e32 v118, v118
	v_add_f32_e32 v126, 1.0, v127
	v_rcp_f32_e32 v126, v126
	v_mul_f32_e32 v115, v119, v115
	v_cndmask_b32_e32 v116, v116, v118, vcc
	v_mul_f32_e32 v119, v120, v116
	v_cndmask_b32_e32 v116, v117, v126, vcc
	v_mul_f32_e32 v120, v121, v116
	v_cvt_pk_f16_f32 v116, v122, v123
	v_mul_f32_e32 v122, 0xbfb8aa3b, v106
	v_exp_f32_e32 v122, v122
	v_mul_f32_e32 v123, 0xbfb8aa3b, v107
	v_exp_f32_e32 v123, v123
	v_cvt_pk_f16_f32 v118, v114, v115
	v_add_f32_e32 v122, 1.0, v122
	v_rcp_f32_e32 v122, v122
	v_mov_b64_e32 v[114:115], s[76:77]
	v_mul_f32_e32 v125, v129, v125
	v_cvt_pk_f16_f32 v119, v119, v120
	v_mad_i64_i32 v[120:121], s[2:3], v154, s42, v[114:115]
	v_lshlrev_b32_e32 v138, 1, v138
	v_cvt_pk_f16_f32 v117, v124, v125
	v_lshl_add_u64 v[120:121], v[120:121], 0, v[138:139]
	v_add_f32_e32 v123, 1.0, v123
	v_cndmask_b32_e32 v106, v106, v122, vcc
	v_rcp_f32_e32 v123, v123
	global_store_dwordx4 v[120:121], v[116:119], off sc0 sc1
	v_mul_f32_e32 v106, v110, v106
	v_mul_f32_e32 v110, 0xbfb8aa3b, v108
	v_mul_f32_e32 v116, 0xbfb8aa3b, v109
	v_exp_f32_e32 v110, v110
	v_exp_f32_e32 v116, v116
	v_cndmask_b32_e32 v107, v107, v123, vcc
	v_mul_f32_e32 v107, v111, v107
	v_add_f32_e32 v110, 1.0, v110
	v_add_f32_e32 v111, 1.0, v116
	v_mul_f32_e32 v116, 0xbfb8aa3b, v98
	v_rcp_f32_e32 v110, v110
	v_exp_f32_e32 v116, v116
	v_rcp_f32_e32 v111, v111
	v_cndmask_b32_e32 v108, v108, v110, vcc
	v_add_f32_e32 v110, 1.0, v116
	v_cndmask_b32_e32 v109, v109, v111, vcc
	v_rcp_f32_e32 v110, v110
	v_mul_f32_e32 v111, 0xbfb8aa3b, v99
	v_exp_f32_e32 v111, v111
	v_mul_f32_e32 v108, v112, v108
	v_cndmask_b32_e32 v98, v98, v110, vcc
	v_mul_f32_e32 v102, v102, v98
	v_add_f32_e32 v98, 1.0, v111
	v_mul_f32_e32 v110, 0xbfb8aa3b, v100
	v_rcp_f32_e32 v98, v98
	v_exp_f32_e32 v110, v110
	v_mul_f32_e32 v111, 0xbfb8aa3b, v101
	v_exp_f32_e32 v111, v111
	v_cndmask_b32_e32 v98, v99, v98, vcc
	v_add_f32_e32 v99, 1.0, v110
	v_rcp_f32_e32 v99, v99
	v_add_f32_e32 v110, 1.0, v111
	v_rcp_f32_e32 v110, v110
	v_mul_f32_e32 v103, v103, v98
	v_cndmask_b32_e32 v98, v100, v99, vcc
	v_mul_f32_e32 v104, v104, v98
	v_cndmask_b32_e32 v98, v101, v110, vcc
	v_mul_f32_e32 v101, v105, v98
	v_cvt_pk_f16_f32 v101, v104, v101
	v_mul_f32_e32 v104, 0xbfb8aa3b, v90
	v_exp_f32_e32 v104, v104
	v_mul_f32_e32 v105, 0xbfb8aa3b, v91
	v_exp_f32_e32 v105, v105
	v_cvt_pk_f16_f32 v100, v102, v103
	v_add_f32_e32 v104, 1.0, v104
	v_rcp_f32_e32 v104, v104
	v_or_b32_e32 v102, 16, v154
	v_mul_f32_e32 v109, v113, v109
	v_mad_i64_i32 v[102:103], s[2:3], v102, s42, v[114:115]
	v_cvt_pk_f16_f32 v98, v106, v107
	v_cvt_pk_f16_f32 v99, v108, v109
	v_lshl_add_u64 v[102:103], v[102:103], 0, v[138:139]
	v_add_f32_e32 v105, 1.0, v105
	v_cndmask_b32_e32 v90, v90, v104, vcc
	v_rcp_f32_e32 v105, v105
	global_store_dwordx4 v[102:103], v[98:101], off sc0 sc1
	v_mul_f32_e32 v90, v94, v90
	v_mul_f32_e32 v94, 0xbfb8aa3b, v92
	v_mul_f32_e32 v98, 0xbfb8aa3b, v93
	v_exp_f32_e32 v94, v94
	v_exp_f32_e32 v98, v98
	v_cndmask_b32_e32 v91, v91, v105, vcc
	v_mul_f32_e32 v91, v95, v91
	v_add_f32_e32 v94, 1.0, v94
	v_add_f32_e32 v95, 1.0, v98
	v_mul_f32_e32 v98, 0xbfb8aa3b, v82
	v_rcp_f32_e32 v94, v94
	v_exp_f32_e32 v98, v98
	v_rcp_f32_e32 v95, v95
	v_cndmask_b32_e32 v92, v92, v94, vcc
	v_add_f32_e32 v94, 1.0, v98
	v_cndmask_b32_e32 v93, v93, v95, vcc
	v_rcp_f32_e32 v94, v94
	v_mul_f32_e32 v95, 0xbfb8aa3b, v83
	v_exp_f32_e32 v95, v95
	v_mul_f32_e32 v92, v96, v92
	v_cndmask_b32_e32 v82, v82, v94, vcc
	v_mul_f32_e32 v86, v86, v82
	v_add_f32_e32 v82, 1.0, v95
	v_mul_f32_e32 v94, 0xbfb8aa3b, v84
	v_rcp_f32_e32 v82, v82
	v_exp_f32_e32 v94, v94
	v_mul_f32_e32 v95, 0xbfb8aa3b, v85
	v_exp_f32_e32 v95, v95
	v_cndmask_b32_e32 v82, v83, v82, vcc
	v_add_f32_e32 v83, 1.0, v94
	v_rcp_f32_e32 v83, v83
	v_add_f32_e32 v94, 1.0, v95
	v_rcp_f32_e32 v94, v94
	v_mul_f32_e32 v87, v87, v82
	v_cndmask_b32_e32 v82, v84, v83, vcc
	v_mul_f32_e32 v88, v88, v82
	v_cndmask_b32_e32 v82, v85, v94, vcc
	v_mul_f32_e32 v85, v89, v82
	v_cvt_pk_f16_f32 v85, v88, v85
	v_mul_f32_e32 v88, 0xbfb8aa3b, v74
	v_exp_f32_e32 v88, v88
	v_mul_f32_e32 v89, 0xbfb8aa3b, v75
	v_exp_f32_e32 v89, v89
	v_cvt_pk_f16_f32 v84, v86, v87
	v_add_f32_e32 v88, 1.0, v88
;     __device__ __forceinline__ void operator()(const Acc& acc, const Unit& u, int wr, int wc, int fr, int fq) const {
;     ...
;         if (u.pn < 8) {
;             const int col0 = (u.pn < 4 ? 0 : 512) + 128 * (u.pn & 3) + wc * 32 + 8 * fq; const bool glu = u.pn >= 4;
; #pragma unroll
;             for (int ai = 0; ai < 2; ++ai)
; #pragma unroll
;                 for (int m = 0; m < 4; ++m) { float h[8];
; #pragma unroll
;                     for (int n = 0; n < 2; ++n)
; #pragma unroll
;                         for (int j = 0; j < 4; ++j) { const float a = acc[ai][0][m][n][j], b = acc[ai][1][m][n][j]; h[n * 4 + j] = glu ? a * __builtin_amdgcn_rcpf(1.f + __builtin_amdgcn_exp2f(-LOG2E * b)) : a * b; }
;                     u32x4 w; w.x = pkh(h[0], h[1]); w.y = pkh(h[2], h[3]); w.z = pkh(h[4], h[5]); w.w = pkh(h[6], h[7]);
;                     *(u32x4*)(O + (size_t)(row0 + ai * HALF + m * 16) * ZP1N + col0) = w; }
	v_rcp_f32_e32 v88, v88
	v_or_b32_e32 v86, 32, v154
	v_mul_f32_e32 v93, v97, v93
	v_mad_i64_i32 v[86:87], s[2:3], v86, s42, v[114:115]
	v_cvt_pk_f16_f32 v82, v90, v91
	v_cvt_pk_f16_f32 v83, v92, v93
	v_lshl_add_u64 v[86:87], v[86:87], 0, v[138:139]
	v_add_f32_e32 v89, 1.0, v89
	v_cndmask_b32_e32 v74, v74, v88, vcc
	v_rcp_f32_e32 v89, v89
	global_store_dwordx4 v[86:87], v[82:85], off sc0 sc1
	v_mul_f32_e32 v74, v78, v74
	v_mul_f32_e32 v78, 0xbfb8aa3b, v76
	v_mul_f32_e32 v82, 0xbfb8aa3b, v77
	v_exp_f32_e32 v78, v78
	v_exp_f32_e32 v82, v82
	v_cndmask_b32_e32 v75, v75, v89, vcc
	v_mul_f32_e32 v75, v79, v75
	v_add_f32_e32 v78, 1.0, v78
	v_add_f32_e32 v79, 1.0, v82
	v_mul_f32_e32 v82, 0xbfb8aa3b, v66
	v_rcp_f32_e32 v78, v78
	v_exp_f32_e32 v82, v82
	v_rcp_f32_e32 v79, v79
	v_cndmask_b32_e32 v76, v76, v78, vcc
	v_add_f32_e32 v78, 1.0, v82
	v_cndmask_b32_e32 v77, v77, v79, vcc
	v_rcp_f32_e32 v78, v78
	v_mul_f32_e32 v79, 0xbfb8aa3b, v67
	v_exp_f32_e32 v79, v79
	v_mul_f32_e32 v76, v80, v76
	v_cndmask_b32_e32 v66, v66, v78, vcc
	v_mul_f32_e32 v70, v70, v66
	v_add_f32_e32 v66, 1.0, v79
	v_mul_f32_e32 v78, 0xbfb8aa3b, v68
	v_rcp_f32_e32 v66, v66
	v_exp_f32_e32 v78, v78
	v_mul_f32_e32 v79, 0xbfb8aa3b, v69
	v_exp_f32_e32 v79, v79
	v_cndmask_b32_e32 v66, v67, v66, vcc
	v_add_f32_e32 v67, 1.0, v78
	v_rcp_f32_e32 v67, v67
	v_add_f32_e32 v78, 1.0, v79
	v_rcp_f32_e32 v78, v78
	v_mul_f32_e32 v71, v71, v66
	v_cndmask_b32_e32 v66, v68, v67, vcc
	v_mul_f32_e32 v72, v72, v66
	v_cndmask_b32_e32 v66, v69, v78, vcc
	v_mul_f32_e32 v69, v73, v66
	v_cvt_pk_f16_f32 v69, v72, v69
	v_mul_f32_e32 v72, 0xbfb8aa3b, v58
	v_exp_f32_e32 v72, v72
	v_cvt_pk_f16_f32 v68, v70, v71
	v_or_b32_e32 v70, 48, v154
	v_mul_f32_e32 v77, v81, v77
	v_mad_i64_i32 v[70:71], s[2:3], v70, s42, v[114:115]
	v_cvt_pk_f16_f32 v66, v74, v75
	v_cvt_pk_f16_f32 v67, v76, v77
	v_lshl_add_u64 v[70:71], v[70:71], 0, v[138:139]
	v_mul_f32_e32 v73, 0xbfb8aa3b, v59
	global_store_dwordx4 v[70:71], v[66:69], off sc0 sc1
	v_exp_f32_e32 v73, v73
	s_nop 0
	v_add_f32_e32 v66, 1.0, v72
	v_rcp_f32_e32 v66, v66
	v_add_f32_e32 v67, 1.0, v73
	v_rcp_f32_e32 v67, v67
	v_add_u32_e32 v68, 0x80, v154
	v_cndmask_b32_e32 v58, v58, v66, vcc
	v_mul_f32_e32 v58, v62, v58
	v_mul_f32_e32 v62, 0xbfb8aa3b, v60
	v_mul_f32_e32 v66, 0xbfb8aa3b, v61
	v_exp_f32_e32 v62, v62
	v_exp_f32_e32 v66, v66
	v_cndmask_b32_e32 v59, v59, v67, vcc
	v_mul_f32_e32 v59, v63, v59
	v_add_f32_e32 v62, 1.0, v62
	v_add_f32_e32 v63, 1.0, v66
	v_mul_f32_e32 v66, 0xbfb8aa3b, v50
	v_rcp_f32_e32 v62, v62
	v_exp_f32_e32 v66, v66
	v_rcp_f32_e32 v63, v63
	v_cndmask_b32_e32 v60, v60, v62, vcc
	v_add_f32_e32 v62, 1.0, v66
	v_cndmask_b32_e32 v61, v61, v63, vcc
	v_rcp_f32_e32 v62, v62
	v_mul_f32_e32 v63, 0xbfb8aa3b, v51
	v_exp_f32_e32 v63, v63
	v_mul_f32_e32 v60, v64, v60
	v_cndmask_b32_e32 v50, v50, v62, vcc
	v_mul_f32_e32 v54, v54, v50
	v_add_f32_e32 v50, 1.0, v63
	v_mul_f32_e32 v62, 0xbfb8aa3b, v52
	v_rcp_f32_e32 v50, v50
	v_exp_f32_e32 v62, v62
	v_mul_f32_e32 v63, 0xbfb8aa3b, v53
	v_exp_f32_e32 v63, v63
	v_cndmask_b32_e32 v50, v51, v50, vcc
	v_add_f32_e32 v51, 1.0, v62
	v_rcp_f32_e32 v51, v51
	v_add_f32_e32 v62, 1.0, v63
	v_rcp_f32_e32 v62, v62
	v_mul_f32_e32 v55, v55, v50
	v_cndmask_b32_e32 v50, v52, v51, vcc
	v_mul_f32_e32 v56, v56, v50
	v_cndmask_b32_e32 v50, v53, v62, vcc
	v_mul_f32_e32 v53, v57, v50
	v_cvt_pk_f16_f32 v53, v56, v53
	v_mul_f32_e32 v56, 0xbfb8aa3b, v42
	v_exp_f32_e32 v56, v56
	v_mul_f32_e32 v57, 0xbfb8aa3b, v43
	v_exp_f32_e32 v57, v57
	v_mul_f32_e32 v61, v65, v61
	v_add_f32_e32 v56, 1.0, v56
	v_rcp_f32_e32 v56, v56
	v_cvt_pk_f16_f32 v52, v54, v55
	v_mad_i64_i32 v[54:55], s[2:3], v68, s42, v[114:115]
	v_cvt_pk_f16_f32 v50, v58, v59
	v_cvt_pk_f16_f32 v51, v60, v61
	v_lshl_add_u64 v[54:55], v[54:55], 0, v[138:139]
	v_add_f32_e32 v57, 1.0, v57
	v_cndmask_b32_e32 v42, v42, v56, vcc
	v_rcp_f32_e32 v57, v57
	global_store_dwordx4 v[54:55], v[50:53], off sc0 sc1
	v_mul_f32_e32 v42, v46, v42
	v_mul_f32_e32 v46, 0xbfb8aa3b, v44
	v_mul_f32_e32 v50, 0xbfb8aa3b, v45
	v_exp_f32_e32 v46, v46
	v_exp_f32_e32 v50, v50
	v_cndmask_b32_e32 v43, v43, v57, vcc
	v_mul_f32_e32 v43, v47, v43
	v_add_f32_e32 v46, 1.0, v46
	v_add_f32_e32 v47, 1.0, v50
	v_mul_f32_e32 v50, 0xbfb8aa3b, v34
	v_rcp_f32_e32 v46, v46
	v_exp_f32_e32 v50, v50
	v_rcp_f32_e32 v47, v47
	v_cndmask_b32_e32 v44, v44, v46, vcc
	v_add_f32_e32 v46, 1.0, v50
	v_cndmask_b32_e32 v45, v45, v47, vcc
	v_rcp_f32_e32 v46, v46
	v_mul_f32_e32 v47, 0xbfb8aa3b, v35
	v_exp_f32_e32 v47, v47
;     __device__ __forceinline__ void operator()(const Acc& acc, const Unit& u, int wr, int wc, int fr, int fq) const {
;     ...
;         if (u.pn < 8) {
;             const int col0 = (u.pn < 4 ? 0 : 512) + 128 * (u.pn & 3) + wc * 32 + 8 * fq; const bool glu = u.pn >= 4;
; #pragma unroll
;             for (int ai = 0; ai < 2; ++ai)
; #pragma unroll
;                 for (int m = 0; m < 4; ++m) { float h[8];
; #pragma unroll
;                     for (int n = 0; n < 2; ++n)
; #pragma unroll
;                         for (int j = 0; j < 4; ++j) { const float a = acc[ai][0][m][n][j], b = acc[ai][1][m][n][j]; h[n * 4 + j] = glu ? a * __builtin_amdgcn_rcpf(1.f + __builtin_amdgcn_exp2f(-LOG2E * b)) : a * b; }
;                     u32x4 w; w.x = pkh(h[0], h[1]); w.y = pkh(h[2], h[3]); w.z = pkh(h[4], h[5]); w.w = pkh(h[6], h[7]);
;                     *(u32x4*)(O + (size_t)(row0 + ai * HALF + m * 16) * ZP1N + col0) = w; }
	v_mul_f32_e32 v44, v48, v44
	v_cndmask_b32_e32 v34, v34, v46, vcc
	v_mul_f32_e32 v38, v38, v34
	v_add_f32_e32 v34, 1.0, v47
	v_mul_f32_e32 v46, 0xbfb8aa3b, v36
	v_rcp_f32_e32 v34, v34
	v_exp_f32_e32 v46, v46
	v_mul_f32_e32 v47, 0xbfb8aa3b, v37
	v_exp_f32_e32 v47, v47
	v_cndmask_b32_e32 v34, v35, v34, vcc
	v_add_f32_e32 v35, 1.0, v46
	v_rcp_f32_e32 v35, v35
	v_add_f32_e32 v46, 1.0, v47
	v_rcp_f32_e32 v46, v46
	v_mul_f32_e32 v39, v39, v34
	v_cndmask_b32_e32 v34, v36, v35, vcc
	v_mul_f32_e32 v40, v40, v34
	v_cndmask_b32_e32 v34, v37, v46, vcc
	v_mul_f32_e32 v37, v41, v34
	v_cvt_pk_f16_f32 v37, v40, v37
	v_mul_f32_e32 v40, 0xbfb8aa3b, v26
	v_exp_f32_e32 v40, v40
	v_mul_f32_e32 v41, 0xbfb8aa3b, v27
	v_exp_f32_e32 v41, v41
	v_cvt_pk_f16_f32 v36, v38, v39
	v_add_f32_e32 v40, 1.0, v40
	v_rcp_f32_e32 v40, v40
	v_add_u32_e32 v38, 0x90, v154
	v_mul_f32_e32 v45, v49, v45
	v_mad_i64_i32 v[38:39], s[2:3], v38, s42, v[114:115]
	v_cvt_pk_f16_f32 v34, v42, v43
	v_cvt_pk_f16_f32 v35, v44, v45
	v_lshl_add_u64 v[38:39], v[38:39], 0, v[138:139]
	v_add_f32_e32 v41, 1.0, v41
	v_cndmask_b32_e32 v26, v26, v40, vcc
	v_rcp_f32_e32 v41, v41
	global_store_dwordx4 v[38:39], v[34:37], off sc0 sc1
	v_mul_f32_e32 v26, v30, v26
	v_mul_f32_e32 v30, 0xbfb8aa3b, v28
	v_mul_f32_e32 v34, 0xbfb8aa3b, v29
	v_exp_f32_e32 v30, v30
	v_exp_f32_e32 v34, v34
	v_cndmask_b32_e32 v27, v27, v41, vcc
	v_mul_f32_e32 v27, v31, v27
	v_add_f32_e32 v30, 1.0, v30
	v_add_f32_e32 v31, 1.0, v34
	v_mul_f32_e32 v34, 0xbfb8aa3b, v18
	v_rcp_f32_e32 v30, v30
	v_exp_f32_e32 v34, v34
	v_rcp_f32_e32 v31, v31
	v_cndmask_b32_e32 v28, v28, v30, vcc
	v_add_f32_e32 v30, 1.0, v34
	v_cndmask_b32_e32 v29, v29, v31, vcc
	v_rcp_f32_e32 v30, v30
	v_mul_f32_e32 v31, 0xbfb8aa3b, v19
	v_exp_f32_e32 v31, v31
	v_mul_f32_e32 v28, v32, v28
	v_cndmask_b32_e32 v18, v18, v30, vcc
	v_mul_f32_e32 v22, v22, v18
	v_add_f32_e32 v18, 1.0, v31
	v_mul_f32_e32 v30, 0xbfb8aa3b, v20
	v_rcp_f32_e32 v18, v18
	v_exp_f32_e32 v30, v30
	v_mul_f32_e32 v31, 0xbfb8aa3b, v21
	v_exp_f32_e32 v31, v31
	v_cndmask_b32_e32 v18, v19, v18, vcc
	v_add_f32_e32 v19, 1.0, v30
	v_rcp_f32_e32 v19, v19
	v_add_f32_e32 v30, 1.0, v31
	v_rcp_f32_e32 v30, v30
	v_mul_f32_e32 v23, v23, v18
	v_cndmask_b32_e32 v18, v20, v19, vcc
	v_mul_f32_e32 v24, v24, v18
	v_cndmask_b32_e32 v18, v21, v30, vcc
	v_mul_f32_e32 v21, v25, v18
	v_cvt_pk_f16_f32 v21, v24, v21
	v_mul_f32_e32 v24, 0xbfb8aa3b, v10
	v_exp_f32_e32 v24, v24
	v_mul_f32_e32 v25, 0xbfb8aa3b, v11
	v_exp_f32_e32 v25, v25
	v_cvt_pk_f16_f32 v20, v22, v23
	v_add_f32_e32 v24, 1.0, v24
	v_rcp_f32_e32 v24, v24
	v_add_u32_e32 v22, 0xa0, v154
	v_mul_f32_e32 v29, v33, v29
	v_mad_i64_i32 v[22:23], s[2:3], v22, s42, v[114:115]
	v_cvt_pk_f16_f32 v18, v26, v27
	v_cvt_pk_f16_f32 v19, v28, v29
	v_lshl_add_u64 v[22:23], v[22:23], 0, v[138:139]
	v_add_f32_e32 v25, 1.0, v25
	v_cndmask_b32_e32 v10, v10, v24, vcc
	v_rcp_f32_e32 v25, v25
	global_store_dwordx4 v[22:23], v[18:21], off sc0 sc1
	v_mul_f32_e32 v10, v14, v10
	v_mul_f32_e32 v14, 0xbfb8aa3b, v12
	v_mul_f32_e32 v18, 0xbfb8aa3b, v13
	v_exp_f32_e32 v14, v14
	v_exp_f32_e32 v18, v18
	v_cndmask_b32_e32 v11, v11, v25, vcc
	v_mul_f32_e32 v11, v15, v11
	v_add_f32_e32 v14, 1.0, v14
	v_add_f32_e32 v15, 1.0, v18
	v_mul_f32_e32 v18, 0xbfb8aa3b, v2
	v_rcp_f32_e32 v14, v14
	v_exp_f32_e32 v18, v18
	v_rcp_f32_e32 v15, v15
	v_cndmask_b32_e32 v12, v12, v14, vcc
	v_add_f32_e32 v14, 1.0, v18
	v_cndmask_b32_e32 v13, v13, v15, vcc
	v_rcp_f32_e32 v14, v14
	v_mul_f32_e32 v15, 0xbfb8aa3b, v3
	v_exp_f32_e32 v15, v15
	v_mul_f32_e32 v12, v16, v12
	v_cndmask_b32_e32 v2, v2, v14, vcc
	v_mul_f32_e32 v6, v6, v2
	v_add_f32_e32 v2, 1.0, v15
	v_mul_f32_e32 v14, 0xbfb8aa3b, v4
	v_rcp_f32_e32 v2, v2
	v_exp_f32_e32 v14, v14
	v_mul_f32_e32 v15, 0xbfb8aa3b, v5
	v_exp_f32_e32 v15, v15
	v_cndmask_b32_e32 v2, v3, v2, vcc
	v_add_f32_e32 v3, 1.0, v14
	v_rcp_f32_e32 v3, v3
	v_add_f32_e32 v14, 1.0, v15
	v_rcp_f32_e32 v14, v14
	v_mul_f32_e32 v7, v7, v2
	v_cndmask_b32_e32 v2, v4, v3, vcc
	v_mul_f32_e32 v8, v8, v2
	v_cndmask_b32_e32 v2, v5, v14, vcc
	v_cvt_pk_f16_f32 v4, v6, v7
	v_add_u32_e32 v6, 0xb0, v154
	v_mul_f32_e32 v13, v17, v13
	v_mul_f32_e32 v5, v9, v2
	v_mad_i64_i32 v[6:7], s[2:3], v6, s42, v[114:115]
	v_cvt_pk_f16_f32 v2, v10, v11
	v_cvt_pk_f16_f32 v3, v12, v13
	v_cvt_pk_f16_f32 v5, v8, v5
	v_lshl_add_u64 v[6:7], v[6:7], 0, v[138:139]
	global_store_dwordx4 v[6:7], v[2:5], off sc0 sc1
	s_andn2_b64 vcc, exec, s[4:5]
	s_mov_b64 s[2:3], -1
	s_cbranch_vccnz .LBB0_1277

;     __device__ __forceinline__ void operator()(const Acc& acc, const Unit& u, int wr, int wc, int fr, int fq) const {
;     ...
;             for (int m = 0; m < 4; ++m) { const int row = row0 + ai * HALF + m * 16; const float s = gv[((row >> 8) * NE + u.g) * CAP + (row & 255)];
;                 f16* rowp = Og + (size_t)row * DM + col0;
; #pragma unroll
;                 for (int bj = 0; bj < 2; ++bj) { const f32x4 v0 = acc[ai][bj][m][0] * s, v1 = acc[ai][bj][m][1] * s;
;                     u32x4 w; w.x = pkh(v0[0], v0[1]); w.y = pkh(v0[2], v0[3]); w.z = pkh(v1[0], v1[1]); w.w = pkh(v1[2], v1[3]);
;                     *(u32x4*)(rowp + bj * HALF) = w; } }
.LBB0_1870:
	v_lshl_add_u32 v148, s49, 8, v1
	v_lshrrev_b32_e32 v146, 4, v148
	v_and_b32_e32 v146, 0xfffff0, v146
	v_add_lshl_u32 v166, v146, s16, 8
	v_or_b32_e32 v146, v166, v151
	v_ashrrev_i32_e32 v147, 31, v146
	v_lshl_add_u64 v[146:147], v[146:147], 2, s[72:73]
	global_load_dword v156, v[146:147], off
	v_lshl_or_b32 v146, s17, 8, v152
	s_ashr_i32 s17, s16, 31
	s_lshl_b64 s[2:3], s[16:17], 23
	s_add_u32 s2, s74, s2
	v_ashrrev_i32_e32 v147, 31, v146
	v_ashrrev_i32_e32 v149, 31, v148
	v_or_b32_e32 v158, 16, v148
	s_addc_u32 s3, s75, s3
	v_lshlrev_b64 v[160:161], 11, v[148:149]
	v_lshl_add_u64 v[146:147], v[146:147], 1, s[2:3]
	v_and_or_b32 v162, v158, s45, v166
	v_lshl_add_u64 v[160:161], v[146:147], 0, v[160:161]
	v_ashrrev_i32_e32 v163, 31, v162
	v_lshl_add_u64 v[162:163], v[162:163], 2, s[72:73]
	v_ashrrev_i32_e32 v159, 31, v158
	s_and_b64 vcc, exec, s[4:5]
	s_mov_b64 s[2:3], -1
	s_waitcnt vmcnt(0)
	v_pk_mul_f32 v[128:129], v[128:129], v[156:157] op_sel_hi:[1,0]
	v_pk_mul_f32 v[126:127], v[126:127], v[156:157] op_sel_hi:[1,0]
	v_pk_mul_f32 v[124:125], v[124:125], v[156:157] op_sel_hi:[1,0]
	v_pk_mul_f32 v[122:123], v[122:123], v[156:157] op_sel_hi:[1,0]
	v_pk_mul_f32 v[120:121], v[120:121], v[156:157] op_sel_hi:[1,0]
	v_pk_mul_f32 v[118:119], v[118:119], v[156:157] op_sel_hi:[1,0]
	v_pk_mul_f32 v[164:165], v[116:117], v[156:157] op_sel_hi:[1,0]
	v_pk_mul_f32 v[156:157], v[114:115], v[156:157] op_sel_hi:[1,0]
	v_cvt_pk_f16_f32 v114, v126, v127
	v_cvt_pk_f16_f32 v115, v128, v129
	v_cvt_pk_f16_f32 v116, v122, v123
	v_cvt_pk_f16_f32 v117, v124, v125
	v_cvt_pk_f16_f32 v118, v118, v119
	v_cvt_pk_f16_f32 v119, v120, v121
	v_cvt_pk_f16_f32 v120, v156, v157
	v_cvt_pk_f16_f32 v121, v164, v165
	global_store_dwordx4 v[160:161], v[114:117], off sc0 sc1
	global_store_dwordx4 v[160:161], v[118:121], off offset:256 sc0 sc1
	global_load_dword v114, v[162:163], off
	v_or_b32_e32 v116, 32, v148
	v_lshlrev_b64 v[118:119], 11, v[158:159]
	v_and_or_b32 v120, v116, s46, v166
	v_lshl_add_u64 v[118:119], v[146:147], 0, v[118:119]
	v_ashrrev_i32_e32 v121, 31, v120
	v_lshl_add_u64 v[120:121], v[120:121], 2, s[72:73]
	v_ashrrev_i32_e32 v117, 31, v116
	s_waitcnt vmcnt(0)
	v_pk_mul_f32 v[112:113], v[112:113], v[114:115] op_sel_hi:[1,0]
	v_pk_mul_f32 v[110:111], v[110:111], v[114:115] op_sel_hi:[1,0]
	v_pk_mul_f32 v[108:109], v[108:109], v[114:115] op_sel_hi:[1,0]
	v_pk_mul_f32 v[106:107], v[106:107], v[114:115] op_sel_hi:[1,0]
	v_pk_mul_f32 v[104:105], v[104:105], v[114:115] op_sel_hi:[1,0]
	v_pk_mul_f32 v[102:103], v[102:103], v[114:115] op_sel_hi:[1,0]
	v_pk_mul_f32 v[122:123], v[100:101], v[114:115] op_sel_hi:[1,0]
	v_pk_mul_f32 v[114:115], v[98:99], v[114:115] op_sel_hi:[1,0]
	v_cvt_pk_f16_f32 v98, v110, v111
	v_cvt_pk_f16_f32 v99, v112, v113
	v_cvt_pk_f16_f32 v100, v106, v107
	v_cvt_pk_f16_f32 v101, v108, v109
	v_cvt_pk_f16_f32 v102, v102, v103
	v_cvt_pk_f16_f32 v103, v104, v105
	v_cvt_pk_f16_f32 v104, v114, v115
	v_cvt_pk_f16_f32 v105, v122, v123
	global_store_dwordx4 v[118:119], v[98:101], off sc0 sc1
	global_store_dwordx4 v[118:119], v[102:105], off offset:256 sc0 sc1
	global_load_dword v98, v[120:121], off
	v_or_b32_e32 v100, 48, v148
	v_lshlrev_b64 v[102:103], 11, v[116:117]
	v_and_or_b32 v104, v100, s47, v166
	v_lshl_add_u64 v[102:103], v[146:147], 0, v[102:103]
	v_ashrrev_i32_e32 v105, 31, v104
	v_lshl_add_u64 v[104:105], v[104:105], 2, s[72:73]
	v_ashrrev_i32_e32 v101, 31, v100
	s_waitcnt vmcnt(0)
	v_pk_mul_f32 v[96:97], v[96:97], v[98:99] op_sel_hi:[1,0]
	v_pk_mul_f32 v[94:95], v[94:95], v[98:99] op_sel_hi:[1,0]
	v_pk_mul_f32 v[92:93], v[92:93], v[98:99] op_sel_hi:[1,0]
	v_pk_mul_f32 v[90:91], v[90:91], v[98:99] op_sel_hi:[1,0]
	v_pk_mul_f32 v[88:89], v[88:89], v[98:99] op_sel_hi:[1,0]
	v_pk_mul_f32 v[86:87], v[86:87], v[98:99] op_sel_hi:[1,0]
	v_pk_mul_f32 v[106:107], v[84:85], v[98:99] op_sel_hi:[1,0]
	v_pk_mul_f32 v[98:99], v[82:83], v[98:99] op_sel_hi:[1,0]
	v_cvt_pk_f16_f32 v82, v94, v95
	v_cvt_pk_f16_f32 v83, v96, v97
	v_cvt_pk_f16_f32 v84, v90, v91
	v_cvt_pk_f16_f32 v85, v92, v93
	v_cvt_pk_f16_f32 v86, v86, v87
	v_cvt_pk_f16_f32 v87, v88, v89
	v_cvt_pk_f16_f32 v88, v98, v99
	v_cvt_pk_f16_f32 v89, v106, v107
	global_store_dwordx4 v[102:103], v[82:85], off sc0 sc1
	global_store_dwordx4 v[102:103], v[86:89], off offset:256 sc0 sc1
	global_load_dword v82, v[104:105], off
	v_add_u32_e32 v84, 0x80, v148
	v_lshrrev_b32_e32 v83, 4, v84
	v_and_b32_e32 v83, 0xfffff0, v83
	v_add_lshl_u32 v92, v83, s16, 8
	v_lshlrev_b64 v[86:87], 11, v[100:101]
	v_and_or_b32 v88, v84, s38, v92
	v_lshl_add_u64 v[86:87], v[146:147], 0, v[86:87]
	v_ashrrev_i32_e32 v89, 31, v88
	v_lshl_add_u64 v[88:89], v[88:89], 2, s[72:73]
	v_ashrrev_i32_e32 v85, 31, v84
	s_waitcnt vmcnt(0)
; #define GM_BAR __builtin_amdgcn_s_barrier()
;     __device__ __forceinline__ void operator()(const Acc& acc, const Unit& u, int wr, int wc, int fr, int fq) const {
;     ...
;             for (int m = 0; m < 4; ++m) { const int row = row0 + ai * HALF + m * 16; const float s = gv[((row >> 8) * NE + u.g) * CAP + (row & 255)];
;                 f16* rowp = Og + (size_t)row * DM + col0;
; #pragma unroll
;                 for (int bj = 0; bj < 2; ++bj) { const f32x4 v0 = acc[ai][bj][m][0] * s, v1 = acc[ai][bj][m][1] * s;
;                     u32x4 w; w.x = pkh(v0[0], v0[1]); w.y = pkh(v0[2], v0[3]); w.z = pkh(v1[0], v1[1]); w.w = pkh(v1[2], v1[3]);
;                     *(u32x4*)(rowp + bj * HALF) = w; } }
; template <bool BF, bool GATHER = false, class Epi, class Hook>
; __device__ __forceinline__ void gemm_phase(LAS unsigned char* lds, const Gemm g, const Order& S, const Epi& E, Hook& HK) {
;     ...
;         cur = nxt; cA = nA; cB = nB; ++ui;
;         if constexpr (GATHER) { gA0[0] = nA0[0]; gA0[1] = nA0[1]; gA1[0] = nA1[0]; gA1[1] = nA1[1]; }
;         if (wr == 1) GM_BAR;
	v_pk_mul_f32 v[80:81], v[80:81], v[82:83] op_sel_hi:[1,0]
	v_pk_mul_f32 v[78:79], v[78:79], v[82:83] op_sel_hi:[1,0]
	v_pk_mul_f32 v[76:77], v[76:77], v[82:83] op_sel_hi:[1,0]
	v_pk_mul_f32 v[74:75], v[74:75], v[82:83] op_sel_hi:[1,0]
	v_pk_mul_f32 v[72:73], v[72:73], v[82:83] op_sel_hi:[1,0]
	v_pk_mul_f32 v[70:71], v[70:71], v[82:83] op_sel_hi:[1,0]
	v_pk_mul_f32 v[90:91], v[68:69], v[82:83] op_sel_hi:[1,0]
	v_pk_mul_f32 v[82:83], v[66:67], v[82:83] op_sel_hi:[1,0]
	v_cvt_pk_f16_f32 v66, v78, v79
	v_cvt_pk_f16_f32 v67, v80, v81
	v_cvt_pk_f16_f32 v68, v74, v75
	v_cvt_pk_f16_f32 v69, v76, v77
	v_cvt_pk_f16_f32 v70, v70, v71
	v_cvt_pk_f16_f32 v71, v72, v73
	v_cvt_pk_f16_f32 v72, v82, v83
	v_cvt_pk_f16_f32 v73, v90, v91
	global_store_dwordx4 v[86:87], v[66:69], off sc0 sc1
	global_store_dwordx4 v[86:87], v[70:73], off offset:256 sc0 sc1
	global_load_dword v66, v[88:89], off
	v_add_u32_e32 v68, 0x90, v148
	v_lshlrev_b64 v[70:71], 11, v[84:85]
	v_and_or_b32 v72, v68, s45, v92
	v_lshl_add_u64 v[70:71], v[146:147], 0, v[70:71]
	v_ashrrev_i32_e32 v73, 31, v72
	v_lshl_add_u64 v[72:73], v[72:73], 2, s[72:73]
	v_ashrrev_i32_e32 v69, 31, v68
	s_waitcnt vmcnt(0)
	v_pk_mul_f32 v[64:65], v[64:65], v[66:67] op_sel_hi:[1,0]
	v_pk_mul_f32 v[62:63], v[62:63], v[66:67] op_sel_hi:[1,0]
	v_pk_mul_f32 v[60:61], v[60:61], v[66:67] op_sel_hi:[1,0]
	v_pk_mul_f32 v[58:59], v[58:59], v[66:67] op_sel_hi:[1,0]
	v_pk_mul_f32 v[56:57], v[56:57], v[66:67] op_sel_hi:[1,0]
	v_pk_mul_f32 v[54:55], v[54:55], v[66:67] op_sel_hi:[1,0]
	v_pk_mul_f32 v[74:75], v[52:53], v[66:67] op_sel_hi:[1,0]
	v_pk_mul_f32 v[66:67], v[50:51], v[66:67] op_sel_hi:[1,0]
	v_cvt_pk_f16_f32 v50, v62, v63
	v_cvt_pk_f16_f32 v51, v64, v65
	v_cvt_pk_f16_f32 v52, v58, v59
	v_cvt_pk_f16_f32 v53, v60, v61
	v_cvt_pk_f16_f32 v54, v54, v55
	v_cvt_pk_f16_f32 v55, v56, v57
	v_cvt_pk_f16_f32 v56, v66, v67
	v_cvt_pk_f16_f32 v57, v74, v75
	global_store_dwordx4 v[70:71], v[50:53], off sc0 sc1
	global_store_dwordx4 v[70:71], v[54:57], off offset:256 sc0 sc1
	global_load_dword v50, v[72:73], off
	v_add_u32_e32 v52, 0xa0, v148
	v_lshlrev_b64 v[54:55], 11, v[68:69]
	v_and_or_b32 v56, v52, s46, v92
	v_lshl_add_u64 v[54:55], v[146:147], 0, v[54:55]
	v_ashrrev_i32_e32 v57, 31, v56
	v_lshl_add_u64 v[56:57], v[56:57], 2, s[72:73]
	v_ashrrev_i32_e32 v53, 31, v52
	s_waitcnt vmcnt(0)
	v_pk_mul_f32 v[48:49], v[48:49], v[50:51] op_sel_hi:[1,0]
	v_pk_mul_f32 v[46:47], v[46:47], v[50:51] op_sel_hi:[1,0]
	v_pk_mul_f32 v[44:45], v[44:45], v[50:51] op_sel_hi:[1,0]
	v_pk_mul_f32 v[42:43], v[42:43], v[50:51] op_sel_hi:[1,0]
	v_pk_mul_f32 v[40:41], v[40:41], v[50:51] op_sel_hi:[1,0]
	v_pk_mul_f32 v[38:39], v[38:39], v[50:51] op_sel_hi:[1,0]
	v_pk_mul_f32 v[58:59], v[36:37], v[50:51] op_sel_hi:[1,0]
	v_pk_mul_f32 v[50:51], v[34:35], v[50:51] op_sel_hi:[1,0]
	v_cvt_pk_f16_f32 v34, v46, v47
	v_cvt_pk_f16_f32 v35, v48, v49
	v_cvt_pk_f16_f32 v36, v42, v43
	v_cvt_pk_f16_f32 v37, v44, v45
	v_cvt_pk_f16_f32 v38, v38, v39
	v_cvt_pk_f16_f32 v39, v40, v41
	v_cvt_pk_f16_f32 v40, v50, v51
	v_cvt_pk_f16_f32 v41, v58, v59
	global_store_dwordx4 v[54:55], v[34:37], off sc0 sc1
	global_store_dwordx4 v[54:55], v[38:41], off offset:256 sc0 sc1
	global_load_dword v34, v[56:57], off
	v_add_u32_e32 v36, 0xb0, v148
	v_lshlrev_b64 v[38:39], 11, v[52:53]
	v_and_or_b32 v40, v36, s47, v92
	v_lshl_add_u64 v[38:39], v[146:147], 0, v[38:39]
	v_ashrrev_i32_e32 v41, 31, v40
	v_lshl_add_u64 v[40:41], v[40:41], 2, s[72:73]
	v_ashrrev_i32_e32 v37, 31, v36
	s_waitcnt vmcnt(0)
	v_pk_mul_f32 v[32:33], v[32:33], v[34:35] op_sel_hi:[1,0]
	v_pk_mul_f32 v[30:31], v[30:31], v[34:35] op_sel_hi:[1,0]
	v_pk_mul_f32 v[28:29], v[28:29], v[34:35] op_sel_hi:[1,0]
	v_pk_mul_f32 v[26:27], v[26:27], v[34:35] op_sel_hi:[1,0]
	v_pk_mul_f32 v[24:25], v[24:25], v[34:35] op_sel_hi:[1,0]
	v_pk_mul_f32 v[22:23], v[22:23], v[34:35] op_sel_hi:[1,0]
	v_pk_mul_f32 v[42:43], v[20:21], v[34:35] op_sel_hi:[1,0]
	v_pk_mul_f32 v[34:35], v[18:19], v[34:35] op_sel_hi:[1,0]
	v_cvt_pk_f16_f32 v18, v30, v31
	v_cvt_pk_f16_f32 v19, v32, v33
	v_cvt_pk_f16_f32 v20, v26, v27
	v_cvt_pk_f16_f32 v21, v28, v29
	v_cvt_pk_f16_f32 v22, v22, v23
	v_cvt_pk_f16_f32 v23, v24, v25
	v_cvt_pk_f16_f32 v24, v34, v35
	v_cvt_pk_f16_f32 v25, v42, v43
	global_store_dwordx4 v[38:39], v[18:21], off sc0 sc1
	global_store_dwordx4 v[38:39], v[22:25], off offset:256 sc0 sc1
	global_load_dword v18, v[40:41], off
	v_lshlrev_b64 v[20:21], 11, v[36:37]
	v_lshl_add_u64 v[20:21], v[146:147], 0, v[20:21]
	s_waitcnt vmcnt(0)
	v_pk_mul_f32 v[16:17], v[16:17], v[18:19] op_sel_hi:[1,0]
	v_pk_mul_f32 v[14:15], v[14:15], v[18:19] op_sel_hi:[1,0]
	v_pk_mul_f32 v[12:13], v[12:13], v[18:19] op_sel_hi:[1,0]
	v_pk_mul_f32 v[10:11], v[10:11], v[18:19] op_sel_hi:[1,0]
	v_pk_mul_f32 v[8:9], v[8:9], v[18:19] op_sel_hi:[1,0]
	v_pk_mul_f32 v[6:7], v[6:7], v[18:19] op_sel_hi:[1,0]
	v_pk_mul_f32 v[22:23], v[4:5], v[18:19] op_sel_hi:[1,0]
	v_pk_mul_f32 v[18:19], v[2:3], v[18:19] op_sel_hi:[1,0]
	v_cvt_pk_f16_f32 v2, v14, v15
	v_cvt_pk_f16_f32 v3, v16, v17
	v_cvt_pk_f16_f32 v4, v10, v11
	v_cvt_pk_f16_f32 v5, v12, v13
	v_cvt_pk_f16_f32 v6, v6, v7
	v_cvt_pk_f16_f32 v7, v8, v9
	v_cvt_pk_f16_f32 v8, v18, v19
	v_cvt_pk_f16_f32 v9, v22, v23
	global_store_dwordx4 v[20:21], v[2:5], off sc0 sc1
	global_store_dwordx4 v[20:21], v[6:9], off offset:256 sc0 sc1
	s_cbranch_vccnz .LBB0_1852
	s_andn2_b64 vcc, exec, s[10:11]
	s_cbranch_vccnz .LBB0_1851
	s_barrier
	s_branch .LBB0_1851
